# s27
# baseline (speedup 1.0000x reference)
.LBB1_5:
	v_lshlrev_b32_e32 v67, 4, v1
	v_lshrrev_b32_e32 v1, 1, v1
	v_lshrrev_b32_e32 v69, 5, v132
	v_ashrrev_i32_e32 v66, 4, v132
	v_bitop3_b32 v1, v1, v69, 7 bitop3:0x78
	s_add_u32 s22, s24, s2
	v_lshlrev_b32_e32 v68, 7, v66
	v_lshlrev_b32_e32 v1, 4, v1
	v_and_b32_e32 v0, 8, v0
	s_addc_u32 s90, s25, s3
	v_lshl_or_b32 v201, v66, 12, v67
	v_or3_b32 v0, v68, v1, v0
	v_add_u32_e32 v100, 0x10000, v0
	v_cvt_pk_f16_f32 v1, v64, v65
	v_cvt_pk_f16_f32 v0, v62, v63
	v_cvt_pk_f16_f32 v61, v60, v61
	v_cvt_pk_f16_f32 v60, v58, v59
	ds_write2st64_b64 v100, v[0:1], v[60:61] offset1:8
	v_cvt_pk_f16_f32 v1, v56, v57
	v_cvt_pk_f16_f32 v0, v54, v55
	v_cvt_pk_f16_f32 v53, v52, v53
	v_cvt_pk_f16_f32 v52, v50, v51
	ds_write2st64_b64 v100, v[0:1], v[52:53] offset0:16 offset1:24
	v_cvt_pk_f16_f32 v1, v48, v49
	v_cvt_pk_f16_f32 v0, v46, v47
	v_cvt_pk_f16_f32 v45, v44, v45
	v_cvt_pk_f16_f32 v44, v42, v43
	ds_write2st64_b64 v100, v[0:1], v[44:45] offset0:32 offset1:40
	v_cvt_pk_f16_f32 v1, v40, v41
	v_cvt_pk_f16_f32 v0, v38, v39
	v_cvt_pk_f16_f32 v37, v36, v37
	v_cvt_pk_f16_f32 v36, v34, v35
	ds_write2st64_b64 v100, v[0:1], v[36:37] offset0:48 offset1:56
	s_add_u32 s0, s22, 0x200
	s_addc_u32 s1, s90, 0
	s_add_u32 s70, s0, 0x20000
	s_addc_u32 s71, s1, 0
	s_add_u32 s72, s0, 0x40000
	s_addc_u32 s73, s1, 0
	s_add_u32 s92, s0, 0x60000
	s_addc_u32 s93, s1, 0
	s_add_u32 s94, s0, 0x80000
	s_addc_u32 s95, s1, 0
	s_add_u32 s96, s0, 0xa0000
	s_addc_u32 s97, s1, 0
	s_add_u32 s98, s0, 0xc0000
	s_addc_u32 s99, s1, 0
	s_add_u32 s80, s0, 0xe0000
	s_addc_u32 s81, s1, 0
	global_load_dwordx4 v[70:73], v201, s[0:1] nt
	global_load_dwordx4 v[42:45], v201, s[70:71] nt
	global_load_dwordx4 v[46:49], v201, s[72:73] nt
	global_load_dwordx4 v[66:69], v201, s[92:93] nt
	global_load_dwordx4 v[62:65], v201, s[94:95] nt
	global_load_dwordx4 v[58:61], v201, s[96:97] nt
	global_load_dwordx4 v[54:57], v201, s[98:99] nt
	global_load_dwordx4 v[50:53], v201, s[80:81] nt
	s_waitcnt vmcnt(8)
	s_waitcnt lgkmcnt(0)
	s_barrier
	ds_read_b128 v[34:37], v131
	ds_read_b128 v[38:41], v131 offset:2048
	ds_read_b128 v[74:77], v131 offset:4096
	ds_read_b128 v[78:81], v131 offset:6144
	ds_read_b128 v[82:85], v129
	ds_read_b128 v[86:89], v129 offset:2048
	s_add_u32 s70, s22, 0x300
	v_add_u32_e32 v95, 0x8000, v94
	v_lshl_add_u64 v[0:1], s[26:27], 0, v[196:197]
	s_addc_u32 s71, s90, 0
	v_readfirstlane_b32 s0, v95
	s_mov_b32 m0, s0
	v_cvt_pk_f16_f32 v33, v32, v33
	global_load_lds_dwordx4 v[0:1], off
	v_cvt_pk_f16_f32 v32, v30, v31
	ds_write_b64 v100, v[32:33] offset:32768
	global_load_dwordx4 v[30:33], v201, s[70:71] nt
	s_setprio 1
	s_waitcnt lgkmcnt(1)
	v_mfma_f32_16x16x32_f16 v[90:93], v[82:85], v[34:37], 0
	v_mfma_f32_16x16x32_f16 v[102:105], v[82:85], v[38:41], 0
	v_mfma_f32_16x16x32_f16 v[106:109], v[82:85], v[74:77], 0
	v_mfma_f32_16x16x32_f16 v[82:85], v[82:85], v[78:81], 0
	v_mfma_f32_16x16x32_f16 v[110:113], v[86:89], v[34:37], 0
	v_mfma_f32_16x16x32_f16 v[114:117], v[86:89], v[38:41], 0
	v_mfma_f32_16x16x32_f16 v[118:121], v[86:89], v[74:77], 0
	v_mfma_f32_16x16x32_f16 v[86:89], v[86:89], v[78:81], 0
	s_setprio 0
	ds_read_b128 v[122:125], v129 offset:4096
	ds_read_b128 v[134:137], v129 offset:6144
	v_add_u32_e32 v96, 0xa000, v94
	v_lshl_add_u64 v[98:99], v[0:1], 0, s[58:59]
	v_readfirstlane_b32 s1, v96
	s_mov_b32 m0, s1
	v_cvt_pk_f16_f32 v29, v28, v29
	global_load_lds_dwordx4 v[98:99], off
	v_cvt_pk_f16_f32 v28, v26, v27
	ds_write_b64 v100, v[28:29] offset:36864
	s_add_u32 s70, s22, 0x20300
	s_addc_u32 s71, s90, 0
	global_load_dwordx4 v[26:29], v201, s[70:71] nt
	s_setprio 1
	s_waitcnt lgkmcnt(1)
	v_mfma_f32_16x16x32_f16 v[138:141], v[122:125], v[34:37], 0
	v_mfma_f32_16x16x32_f16 v[142:145], v[122:125], v[38:41], 0
	v_mfma_f32_16x16x32_f16 v[146:149], v[122:125], v[74:77], 0
	v_mfma_f32_16x16x32_f16 v[122:125], v[122:125], v[78:81], 0
	v_mfma_f32_16x16x32_f16 v[150:153], v[134:137], v[34:37], 0
	v_mfma_f32_16x16x32_f16 v[154:157], v[134:137], v[38:41], 0
	v_mfma_f32_16x16x32_f16 v[158:161], v[134:137], v[74:77], 0
	v_mfma_f32_16x16x32_f16 v[134:137], v[134:137], v[78:81], 0
	s_setprio 0
	ds_read_b128 v[162:165], v129 offset:8192
	ds_read_b128 v[166:169], v129 offset:10240
	v_add_u32_e32 v97, 0xc000, v94
	v_lshl_add_u64 v[98:99], v[0:1], 0, s[60:61]
	v_readfirstlane_b32 s71, v97
	s_mov_b32 m0, s71
	v_cvt_pk_f16_f32 v25, v24, v25
	global_load_lds_dwordx4 v[98:99], off
	v_lshl_add_u64 v[252:253], v[0:1], 0, s[62:63]
	s_add_u32 m0, m0, 0x2000
	s_nop 0
	global_load_lds_dwordx4 v[252:253], off
	v_cvt_pk_f16_f32 v24, v22, v23
	ds_write_b64 v100, v[24:25] offset:40960
	s_add_u32 s72, s22, 0x40300
	s_addc_u32 s73, s90, 0
	global_load_dwordx4 v[22:25], v201, s[72:73] nt
	s_setprio 1
	s_waitcnt lgkmcnt(1)
	v_mfma_f32_16x16x32_f16 v[170:173], v[162:165], v[34:37], 0
	v_mfma_f32_16x16x32_f16 v[174:177], v[162:165], v[38:41], 0
	v_mfma_f32_16x16x32_f16 v[178:181], v[162:165], v[74:77], 0
	v_mfma_f32_16x16x32_f16 v[162:165], v[162:165], v[78:81], 0
	v_mfma_f32_16x16x32_f16 v[182:185], v[166:169], v[34:37], 0
	v_mfma_f32_16x16x32_f16 v[186:189], v[166:169], v[38:41], 0
	v_mfma_f32_16x16x32_f16 v[190:193], v[166:169], v[74:77], 0
	v_mfma_f32_16x16x32_f16 v[166:169], v[166:169], v[78:81], 0
	s_setprio 0
	ds_read_b128 v[202:205], v129 offset:12288
	ds_read_b128 v[206:209], v129 offset:14336
	v_add_u32_e32 v98, 0xe000, v94
	v_lshl_add_u64 v[0:1], v[0:1], 0, s[62:63]
	v_readfirstlane_b32 s72, v98
	v_cvt_pk_f16_f32 v1, v20, v21
	v_cvt_pk_f16_f32 v0, v18, v19
	ds_write_b64 v100, v[0:1] offset:45056
	s_add_u32 s80, s22, 0x60300
	s_addc_u32 s81, s90, 0
	global_load_dwordx4 v[18:21], v201, s[80:81] nt
	s_setprio 1
	s_waitcnt lgkmcnt(1)
	v_mfma_f32_16x16x32_f16 v[210:213], v[202:205], v[34:37], 0
	v_mfma_f32_16x16x32_f16 v[214:217], v[202:205], v[38:41], 0
	v_mfma_f32_16x16x32_f16 v[218:221], v[202:205], v[74:77], 0
	v_mfma_f32_16x16x32_f16 v[202:205], v[202:205], v[78:81], 0
	v_mfma_f32_16x16x32_f16 v[74:77], v[206:209], v[74:77], 0
	v_mfma_f32_16x16x32_f16 v[78:81], v[206:209], v[78:81], 0
	v_mfma_f32_16x16x32_f16 v[222:225], v[206:209], v[34:37], 0
	v_mfma_f32_16x16x32_f16 v[226:229], v[206:209], v[38:41], 0
	s_setprio 0
	ds_read_b128 v[206:209], v128
	ds_read_b128 v[230:233], v128 offset:2048
	ds_read_b128 v[234:237], v128 offset:4096
	ds_read_b128 v[238:241], v128 offset:6144
	ds_read_b128 v[34:37], v130
	ds_read_b128 v[38:41], v130 offset:2048
	v_cvt_pk_f16_f32 v1, v16, v17
	v_cvt_pk_f16_f32 v0, v14, v15
	ds_write_b64 v100, v[0:1] offset:49152
	s_add_u32 s80, s22, 0x80300
	s_addc_u32 s81, s90, 0
	global_load_dwordx4 v[14:17], v201, s[80:81] nt
	s_setprio 1
	s_waitcnt lgkmcnt(1)
	v_mfma_f32_16x16x32_f16 v[90:93], v[34:37], v[206:209], v[90:93]
	v_mfma_f32_16x16x32_f16 v[102:105], v[34:37], v[230:233], v[102:105]
	v_mfma_f32_16x16x32_f16 v[106:109], v[34:37], v[234:237], v[106:109]
	v_mfma_f32_16x16x32_f16 v[82:85], v[34:37], v[238:241], v[82:85]
	v_mfma_f32_16x16x32_f16 v[110:113], v[38:41], v[206:209], v[110:113]
	v_mfma_f32_16x16x32_f16 v[114:117], v[38:41], v[230:233], v[114:117]
	v_mfma_f32_16x16x32_f16 v[118:121], v[38:41], v[234:237], v[118:121]
	v_mfma_f32_16x16x32_f16 v[86:89], v[38:41], v[238:241], v[86:89]
	s_setprio 0
	ds_read_b128 v[34:37], v130 offset:4096
	ds_read_b128 v[38:41], v130 offset:6144
	v_cvt_pk_f16_f32 v1, v12, v13
	v_cvt_pk_f16_f32 v0, v10, v11
	ds_write_b64 v100, v[0:1] offset:53248
	s_add_u32 s80, s22, 0xa0300
	s_addc_u32 s81, s90, 0
	global_load_dwordx4 v[10:13], v201, s[80:81] nt
	s_setprio 1
	s_waitcnt lgkmcnt(1)
	v_mfma_f32_16x16x32_f16 v[146:149], v[34:37], v[234:237], v[146:149]
	v_mfma_f32_16x16x32_f16 v[122:125], v[34:37], v[238:241], v[122:125]
	v_mfma_f32_16x16x32_f16 v[134:137], v[38:41], v[238:241], v[134:137]
	v_mfma_f32_16x16x32_f16 v[138:141], v[34:37], v[206:209], v[138:141]
	v_mfma_f32_16x16x32_f16 v[142:145], v[34:37], v[230:233], v[142:145]
	v_mfma_f32_16x16x32_f16 v[150:153], v[38:41], v[206:209], v[150:153]
	v_mfma_f32_16x16x32_f16 v[154:157], v[38:41], v[230:233], v[154:157]
	v_mfma_f32_16x16x32_f16 v[158:161], v[38:41], v[234:237], v[158:161]
	s_setprio 0
	ds_read_b128 v[38:41], v130 offset:8192
	ds_read_b128 v[242:245], v130 offset:10240
	v_cvt_pk_f16_f32 v1, v8, v9
	v_cvt_pk_f16_f32 v0, v6, v7
	ds_write_b64 v100, v[0:1] offset:57344
	s_add_u32 s80, s22, 0xc0300
	s_addc_u32 s81, s90, 0
	global_load_dwordx4 v[34:37], v201, s[80:81] nt
	s_setprio 1
	s_waitcnt lgkmcnt(1)
	v_mfma_f32_16x16x32_f16 v[6:9], v[38:41], v[206:209], v[170:173]
	v_mfma_f32_16x16x32_f16 v[170:173], v[38:41], v[230:233], v[174:177]
	v_mfma_f32_16x16x32_f16 v[174:177], v[38:41], v[234:237], v[178:181]
	v_mfma_f32_16x16x32_f16 v[162:165], v[38:41], v[238:241], v[162:165]
	v_mfma_f32_16x16x32_f16 v[178:181], v[242:245], v[206:209], v[182:185]
	v_mfma_f32_16x16x32_f16 v[182:185], v[242:245], v[230:233], v[186:189]
	v_mfma_f32_16x16x32_f16 v[186:189], v[242:245], v[234:237], v[190:193]
	v_mfma_f32_16x16x32_f16 v[166:169], v[242:245], v[238:241], v[166:169]
	s_setprio 0
	s_nop 0
	ds_read_b128 v[190:193], v130 offset:12288
	ds_read_b128 v[242:245], v130 offset:14336
	v_cvt_pk_f16_f32 v1, v4, v5
	v_cvt_pk_f16_f32 v0, v2, v3
	ds_write_b64 v100, v[0:1] offset:61440
	s_add_u32 s80, s22, 0xe0300
	s_addc_u32 s81, s90, 0
	global_load_dwordx4 v[38:41], v201, s[80:81] nt
	s_setprio 1
	s_waitcnt lgkmcnt(1)
	v_mfma_f32_16x16x32_f16 v[78:81], v[242:245], v[238:241], v[78:81]
	v_mfma_f32_16x16x32_f16 v[210:213], v[190:193], v[206:209], v[210:213]
	v_mfma_f32_16x16x32_f16 v[214:217], v[190:193], v[230:233], v[214:217]
	v_mfma_f32_16x16x32_f16 v[218:221], v[190:193], v[234:237], v[218:221]
	v_mfma_f32_16x16x32_f16 v[190:193], v[190:193], v[238:241], v[202:205]
	v_mfma_f32_16x16x32_f16 v[202:205], v[242:245], v[206:209], v[222:225]
	v_mfma_f32_16x16x32_f16 v[206:209], v[242:245], v[230:233], v[226:229]
	v_mfma_f32_16x16x32_f16 v[222:225], v[242:245], v[234:237], v[74:77]
	s_setprio 0
	s_waitcnt vmcnt(6)
	s_waitcnt lgkmcnt(0)
	s_barrier
	ds_read_b128 v[226:229], v131 offset:32768
	ds_read_b128 v[230:233], v131 offset:34816
	ds_read_b128 v[234:237], v131 offset:36864
	ds_read_b128 v[238:241], v131 offset:38912
	ds_read_b128 v[74:77], v129 offset:32768
	ds_read_b128 v[242:245], v129 offset:34816
	s_add_u32 s80, s22, 0x400
	s_addc_u32 s81, s90, 0
	v_lshl_add_u64 v[198:199], s[28:29], 0, v[196:197]
	v_readfirstlane_b32 s70, v94
	s_mov_b32 m0, s70
	v_cvt_pk_f16_f32 v1, v72, v73
	global_load_lds_dwordx4 v[198:199], off
	v_cvt_pk_f16_f32 v0, v70, v71
	ds_write_b64 v100, v[0:1]
	global_load_dwordx4 v[0:3], v201, s[80:81] nt
	s_setprio 1
	s_waitcnt lgkmcnt(1)
	v_mfma_f32_16x16x32_f16 v[70:73], v[74:77], v[226:229], v[90:93]
	v_mfma_f32_16x16x32_f16 v[90:93], v[74:77], v[230:233], v[102:105]
	v_mfma_f32_16x16x32_f16 v[104:107], v[74:77], v[234:237], v[106:109]
	v_mfma_f32_16x16x32_f16 v[82:85], v[74:77], v[238:241], v[82:85]
	v_mfma_f32_16x16x32_f16 v[108:111], v[242:245], v[226:229], v[110:113]
	v_mfma_f32_16x16x32_f16 v[112:115], v[242:245], v[230:233], v[114:117]
	v_mfma_f32_16x16x32_f16 v[116:119], v[242:245], v[234:237], v[118:121]
	v_mfma_f32_16x16x32_f16 v[86:89], v[242:245], v[238:241], v[86:89]
	s_setprio 0
	ds_read_b128 v[74:77], v129 offset:36864
	ds_read_b128 v[242:245], v129 offset:38912
	v_add_u32_e32 v99, 0x2000, v94
	v_lshl_add_u64 v[4:5], v[198:199], 0, s[58:59]
	v_readfirstlane_b32 s73, v99
	s_mov_b32 m0, s73
	s_nop 0
	global_load_lds_dwordx4 v[4:5], off
	v_cvt_pk_f16_f32 v5, v44, v45
	v_cvt_pk_f16_f32 v4, v42, v43
	ds_write_b64 v100, v[4:5] offset:4096
	s_add_u32 s80, s22, 0x20400
	s_addc_u32 s81, s90, 0
	global_load_dwordx4 v[42:45], v201, s[80:81] nt
	s_setprio 1
	s_waitcnt lgkmcnt(1)
	v_mfma_f32_16x16x32_f16 v[146:149], v[74:77], v[234:237], v[146:149]
	v_mfma_f32_16x16x32_f16 v[120:123], v[74:77], v[238:241], v[122:125]
	v_mfma_f32_16x16x32_f16 v[124:127], v[242:245], v[226:229], v[150:153]
	v_mfma_f32_16x16x32_f16 v[134:137], v[242:245], v[238:241], v[134:137]
	v_mfma_f32_16x16x32_f16 v[138:141], v[74:77], v[226:229], v[138:141]
	v_mfma_f32_16x16x32_f16 v[142:145], v[74:77], v[230:233], v[142:145]
	v_mfma_f32_16x16x32_f16 v[150:153], v[242:245], v[230:233], v[154:157]
	v_mfma_f32_16x16x32_f16 v[154:157], v[242:245], v[234:237], v[158:161]
	s_setprio 0
	ds_read_b128 v[74:77], v129 offset:40960
	s_nop 0
	ds_read_b128 v[158:161], v129 offset:43008
	v_add_u32_e32 v101, 0x4000, v94
	v_lshl_add_u64 v[4:5], v[198:199], 0, s[60:61]
	v_readfirstlane_b32 s91, v101
	s_mov_b32 m0, s91
	s_nop 0
	global_load_lds_dwordx4 v[4:5], off
	v_lshl_add_u64 v[252:253], v[198:199], 0, s[62:63]
	s_add_u32 m0, m0, 0x2000
	s_nop 0
	global_load_lds_dwordx4 v[252:253], off
	v_cvt_pk_f16_f32 v5, v48, v49
	v_cvt_pk_f16_f32 v4, v46, v47
	ds_write_b64 v100, v[4:5] offset:8192
	s_add_u32 s80, s22, 0x40400
	s_addc_u32 s81, s90, 0
	global_load_dwordx4 v[46:49], v201, s[80:81] nt
	s_setprio 1
	s_waitcnt lgkmcnt(1)
	v_mfma_f32_16x16x32_f16 v[4:7], v[74:77], v[226:229], v[6:9]
	v_mfma_f32_16x16x32_f16 v[170:173], v[74:77], v[230:233], v[170:173]
	v_mfma_f32_16x16x32_f16 v[174:177], v[74:77], v[234:237], v[174:177]
	v_mfma_f32_16x16x32_f16 v[162:165], v[74:77], v[238:241], v[162:165]
	v_mfma_f32_16x16x32_f16 v[178:181], v[158:161], v[226:229], v[178:181]
	v_mfma_f32_16x16x32_f16 v[182:185], v[158:161], v[230:233], v[182:185]
	v_mfma_f32_16x16x32_f16 v[186:189], v[158:161], v[234:237], v[186:189]
	v_mfma_f32_16x16x32_f16 v[158:161], v[158:161], v[238:241], v[166:169]
	s_setprio 0
	s_nop 1
	ds_read_b128 v[166:169], v129 offset:45056
	ds_read_b128 v[242:245], v129 offset:47104
	v_add_u32_e32 v102, 0x6000, v94
	v_lshl_add_u64 v[8:9], v[198:199], 0, s[62:63]
	v_readfirstlane_b32 s92, v102
	v_cvt_pk_f16_f32 v9, v68, v69
	v_cvt_pk_f16_f32 v8, v66, v67
	ds_write_b64 v100, v[8:9] offset:12288
	s_add_u32 s80, s22, 0x60400
	s_addc_u32 s81, s90, 0
	global_load_dwordx4 v[74:77], v201, s[80:81] nt
	s_setprio 1
	s_waitcnt lgkmcnt(1)
	v_mfma_f32_16x16x32_f16 v[66:69], v[166:169], v[226:229], v[210:213]
	v_mfma_f32_16x16x32_f16 v[210:213], v[166:169], v[230:233], v[214:217]
	v_mfma_f32_16x16x32_f16 v[214:217], v[166:169], v[234:237], v[218:221]
	v_mfma_f32_16x16x32_f16 v[166:169], v[166:169], v[238:241], v[190:193]
	v_mfma_f32_16x16x32_f16 v[190:193], v[242:245], v[226:229], v[202:205]
	v_mfma_f32_16x16x32_f16 v[202:205], v[242:245], v[230:233], v[206:209]
	v_mfma_f32_16x16x32_f16 v[206:209], v[242:245], v[234:237], v[222:225]
	v_mfma_f32_16x16x32_f16 v[218:221], v[242:245], v[238:241], v[78:81]
	s_setprio 0
	s_nop 0
	ds_read_b128 v[222:225], v128 offset:32768
	ds_read_b128 v[226:229], v128 offset:34816
	ds_read_b128 v[230:233], v128 offset:36864
	ds_read_b128 v[234:237], v128 offset:38912
	ds_read_b128 v[238:241], v130 offset:32768
	ds_read_b128 v[242:245], v130 offset:34816
	v_cvt_pk_f16_f32 v9, v64, v65
	v_cvt_pk_f16_f32 v8, v62, v63
	ds_write_b64 v100, v[8:9] offset:16384
	s_add_u32 s80, s22, 0x80400
	s_addc_u32 s81, s90, 0
	global_load_dwordx4 v[78:81], v201, s[80:81] nt
	s_setprio 1
	s_waitcnt lgkmcnt(1)
	v_mfma_f32_16x16x32_f16 v[62:65], v[238:241], v[222:225], v[70:73]
	v_mfma_f32_16x16x32_f16 v[70:73], v[238:241], v[226:229], v[90:93]
	v_mfma_f32_16x16x32_f16 v[104:107], v[238:241], v[230:233], v[104:107]
	v_mfma_f32_16x16x32_f16 v[108:111], v[242:245], v[222:225], v[108:111]
	v_mfma_f32_16x16x32_f16 v[112:115], v[242:245], v[226:229], v[112:115]
	v_mfma_f32_16x16x32_f16 v[116:119], v[242:245], v[230:233], v[116:119]
	v_mfma_f32_16x16x32_f16 v[238:241], v[238:241], v[234:237], v[82:85]
	v_mfma_f32_16x16x32_f16 v[242:245], v[242:245], v[234:237], v[86:89]
	s_setprio 0
	s_nop 1
	ds_read_b128 v[86:89], v130 offset:36864
	ds_read_b128 v[90:93], v130 offset:38912
	v_cvt_pk_f16_f32 v9, v60, v61
	v_cvt_pk_f16_f32 v8, v58, v59
	ds_write_b64 v100, v[8:9] offset:20480
	s_add_u32 s80, s22, 0xa0400
	s_addc_u32 s81, s90, 0
	global_load_dwordx4 v[82:85], v201, s[80:81] nt
	s_setprio 1
	s_waitcnt lgkmcnt(1)
	v_mfma_f32_16x16x32_f16 v[58:61], v[86:89], v[222:225], v[138:141]
	v_mfma_f32_16x16x32_f16 v[138:141], v[86:89], v[226:229], v[142:145]
	v_mfma_f32_16x16x32_f16 v[142:145], v[86:89], v[230:233], v[146:149]
	v_mfma_f32_16x16x32_f16 v[120:123], v[86:89], v[234:237], v[120:123]
	v_mfma_f32_16x16x32_f16 v[124:127], v[90:93], v[222:225], v[124:127]
	v_mfma_f32_16x16x32_f16 v[146:149], v[90:93], v[226:229], v[150:153]
	v_mfma_f32_16x16x32_f16 v[134:137], v[90:93], v[234:237], v[134:137]
	v_mfma_f32_16x16x32_f16 v[150:153], v[90:93], v[230:233], v[154:157]
	s_setprio 0
	ds_read_b128 v[90:93], v130 offset:40960
	s_nop 0
	ds_read_b128 v[154:157], v130 offset:43008
	v_cvt_pk_f16_f32 v9, v56, v57
	v_cvt_pk_f16_f32 v8, v54, v55
	ds_write_b64 v100, v[8:9] offset:24576
	s_add_u32 s80, s22, 0xc0400
	s_addc_u32 s81, s90, 0
	global_load_dwordx4 v[86:89], v201, s[80:81] nt
	s_setprio 1
	s_waitcnt lgkmcnt(1)
	v_mfma_f32_16x16x32_f16 v[246:249], v[90:93], v[222:225], v[4:7]
	v_mfma_f32_16x16x32_f16 v[170:173], v[90:93], v[226:229], v[170:173]
	v_mfma_f32_16x16x32_f16 v[174:177], v[90:93], v[230:233], v[174:177]
	v_mfma_f32_16x16x32_f16 v[162:165], v[90:93], v[234:237], v[162:165]
	v_mfma_f32_16x16x32_f16 v[178:181], v[154:157], v[222:225], v[178:181]
	v_mfma_f32_16x16x32_f16 v[182:185], v[154:157], v[226:229], v[182:185]
	v_mfma_f32_16x16x32_f16 v[186:189], v[154:157], v[230:233], v[186:189]
	v_mfma_f32_16x16x32_f16 v[154:157], v[154:157], v[234:237], v[158:161]
	s_setprio 0
	ds_read_b128 v[4:7], v130 offset:45056
	ds_read_b128 v[54:57], v130 offset:47104
	v_cvt_pk_f16_f32 v9, v52, v53
	v_cvt_pk_f16_f32 v8, v50, v51
	ds_write_b64 v100, v[8:9] offset:28672
	s_add_u32 s80, s22, 0xe0400
	s_addc_u32 s81, s90, 0
	global_load_dwordx4 v[90:93], v201, s[80:81] nt
	s_setprio 1
	s_waitcnt lgkmcnt(1)
	v_mfma_f32_16x16x32_f16 v[66:69], v[4:7], v[222:225], v[66:69]
	v_mfma_f32_16x16x32_f16 v[158:161], v[4:7], v[226:229], v[210:213]
	v_mfma_f32_16x16x32_f16 v[210:213], v[4:7], v[230:233], v[214:217]
	v_mfma_f32_16x16x32_f16 v[166:169], v[4:7], v[234:237], v[166:169]
	v_mfma_f32_16x16x32_f16 v[190:193], v[54:57], v[222:225], v[190:193]
	v_mfma_f32_16x16x32_f16 v[202:205], v[54:57], v[226:229], v[202:205]
	v_mfma_f32_16x16x32_f16 v[206:209], v[54:57], v[230:233], v[206:209]
	v_mfma_f32_16x16x32_f16 v[214:217], v[54:57], v[234:237], v[218:221]
	s_setprio 0
	s_waitcnt vmcnt(6)
	s_waitcnt lgkmcnt(0)
	s_barrier
	s_nop 0
	ds_read_b128 v[218:221], v131
	ds_read_b128 v[222:225], v131 offset:2048
	ds_read_b128 v[226:229], v131 offset:4096
	ds_read_b128 v[230:233], v131 offset:6144
	ds_read_b128 v[50:53], v129
	ds_read_b128 v[54:57], v129 offset:2048
	s_add_u32 s80, s22, 0x500
	v_lshl_add_u64 v[8:9], s[30:31], 0, v[196:197]
	s_addc_u32 s81, s90, 0
	s_mov_b32 m0, s0
	v_cvt_pk_f16_f32 v5, v32, v33
	global_load_lds_dwordx4 v[8:9], off
	v_cvt_pk_f16_f32 v4, v30, v31
	ds_write_b64 v100, v[4:5] offset:32768
	global_load_dwordx4 v[4:7], v201, s[80:81] nt
	s_setprio 1
	s_waitcnt lgkmcnt(1)
	v_mfma_f32_16x16x32_f16 v[30:33], v[50:53], v[218:221], v[62:65]
	v_mfma_f32_16x16x32_f16 v[70:73], v[50:53], v[222:225], v[70:73]
	v_mfma_f32_16x16x32_f16 v[104:107], v[50:53], v[226:229], v[104:107]
	v_mfma_f32_16x16x32_f16 v[108:111], v[54:57], v[218:221], v[108:111]
	v_mfma_f32_16x16x32_f16 v[112:115], v[54:57], v[222:225], v[112:115]
	v_mfma_f32_16x16x32_f16 v[116:119], v[54:57], v[226:229], v[116:119]
	v_mfma_f32_16x16x32_f16 v[234:237], v[50:53], v[230:233], v[238:241]
	v_mfma_f32_16x16x32_f16 v[238:241], v[54:57], v[230:233], v[242:245]
	s_setprio 0
	ds_read_b128 v[54:57], v129 offset:4096
	ds_read_b128 v[62:65], v129 offset:6144
	s_mov_b32 m0, s1
	v_lshl_add_u64 v[50:51], v[8:9], 0, s[58:59]
	global_load_lds_dwordx4 v[50:51], off
	v_cvt_pk_f16_f32 v29, v28, v29
	v_cvt_pk_f16_f32 v28, v26, v27
	ds_write_b64 v100, v[28:29] offset:36864
	s_add_u32 s0, s22, 0x20500
	s_addc_u32 s1, s90, 0
	global_load_dwordx4 v[50:53], v201, s[0:1] nt
	s_setprio 1
	s_waitcnt lgkmcnt(1)
	v_mfma_f32_16x16x32_f16 v[26:29], v[54:57], v[218:221], v[58:61]
	v_mfma_f32_16x16x32_f16 v[120:123], v[54:57], v[230:233], v[120:123]
	v_mfma_f32_16x16x32_f16 v[124:127], v[62:65], v[218:221], v[124:127]
	v_mfma_f32_16x16x32_f16 v[146:149], v[62:65], v[222:225], v[146:149]
	v_mfma_f32_16x16x32_f16 v[134:137], v[62:65], v[230:233], v[134:137]
	v_mfma_f32_16x16x32_f16 v[138:141], v[54:57], v[222:225], v[138:141]
	v_mfma_f32_16x16x32_f16 v[142:145], v[54:57], v[226:229], v[142:145]
	v_mfma_f32_16x16x32_f16 v[150:153], v[62:65], v[226:229], v[150:153]
	s_setprio 0
	ds_read_b128 v[58:61], v129 offset:8192
	ds_read_b128 v[62:65], v129 offset:10240
	s_mov_b32 m0, s71
	v_lshl_add_u64 v[54:55], v[8:9], 0, s[60:61]
	global_load_lds_dwordx4 v[54:55], off
	v_lshl_add_u64 v[252:253], v[8:9], 0, s[62:63]
	s_add_u32 m0, m0, 0x2000
	s_nop 0
	global_load_lds_dwordx4 v[252:253], off
	v_cvt_pk_f16_f32 v25, v24, v25
	v_cvt_pk_f16_f32 v24, v22, v23
	ds_write_b64 v100, v[24:25] offset:40960
	s_add_u32 s0, s22, 0x40500
	s_addc_u32 s1, s90, 0
	global_load_dwordx4 v[54:57], v201, s[0:1] nt
	s_setprio 1
	s_waitcnt lgkmcnt(1)
	v_mfma_f32_16x16x32_f16 v[22:25], v[58:61], v[218:221], v[246:249]
	v_mfma_f32_16x16x32_f16 v[170:173], v[58:61], v[222:225], v[170:173]
	v_mfma_f32_16x16x32_f16 v[174:177], v[58:61], v[226:229], v[174:177]
	v_mfma_f32_16x16x32_f16 v[162:165], v[58:61], v[230:233], v[162:165]
	v_mfma_f32_16x16x32_f16 v[178:181], v[62:65], v[218:221], v[178:181]
	v_mfma_f32_16x16x32_f16 v[182:185], v[62:65], v[222:225], v[182:185]
	v_mfma_f32_16x16x32_f16 v[186:189], v[62:65], v[226:229], v[186:189]
	v_mfma_f32_16x16x32_f16 v[154:157], v[62:65], v[230:233], v[154:157]
	s_setprio 0
	ds_read_b128 v[62:65], v129 offset:12288
	ds_read_b128 v[242:245], v129 offset:14336
	v_lshl_add_u64 v[8:9], v[8:9], 0, s[62:63]
	v_cvt_pk_f16_f32 v9, v20, v21
	v_cvt_pk_f16_f32 v8, v18, v19
	ds_write_b64 v100, v[8:9] offset:45056
	s_add_u32 s0, s22, 0x60500
	s_addc_u32 s1, s90, 0
	global_load_dwordx4 v[58:61], v201, s[0:1] nt
	s_setprio 1
	s_waitcnt lgkmcnt(1)
	v_mfma_f32_16x16x32_f16 v[18:21], v[62:65], v[218:221], v[66:69]
	v_mfma_f32_16x16x32_f16 v[158:161], v[62:65], v[222:225], v[158:161]
	v_mfma_f32_16x16x32_f16 v[210:213], v[62:65], v[226:229], v[210:213]
	v_mfma_f32_16x16x32_f16 v[166:169], v[62:65], v[230:233], v[166:169]
	v_mfma_f32_16x16x32_f16 v[190:193], v[242:245], v[218:221], v[190:193]
	v_mfma_f32_16x16x32_f16 v[202:205], v[242:245], v[222:225], v[202:205]
	v_mfma_f32_16x16x32_f16 v[206:209], v[242:245], v[226:229], v[206:209]
	v_mfma_f32_16x16x32_f16 v[214:217], v[242:245], v[230:233], v[214:217]
	s_setprio 0
	ds_read_b128 v[218:221], v128
	ds_read_b128 v[222:225], v128 offset:2048
	ds_read_b128 v[226:229], v128 offset:4096
	ds_read_b128 v[230:233], v128 offset:6144
	ds_read_b128 v[66:69], v130
	ds_read_b128 v[242:245], v130 offset:2048
	v_cvt_pk_f16_f32 v9, v16, v17
	v_cvt_pk_f16_f32 v8, v14, v15
	ds_write_b64 v100, v[8:9] offset:49152
	s_add_u32 s0, s22, 0x80500
	s_addc_u32 s1, s90, 0
	global_load_dwordx4 v[62:65], v201, s[0:1] nt
	s_setprio 1
	s_waitcnt lgkmcnt(1)
	v_mfma_f32_16x16x32_f16 v[14:17], v[66:69], v[218:221], v[30:33]
	v_mfma_f32_16x16x32_f16 v[30:33], v[66:69], v[222:225], v[70:73]
	v_mfma_f32_16x16x32_f16 v[104:107], v[66:69], v[226:229], v[104:107]
	v_mfma_f32_16x16x32_f16 v[108:111], v[242:245], v[218:221], v[108:111]
	v_mfma_f32_16x16x32_f16 v[112:115], v[242:245], v[222:225], v[112:115]
	v_mfma_f32_16x16x32_f16 v[116:119], v[242:245], v[226:229], v[116:119]
	v_mfma_f32_16x16x32_f16 v[234:237], v[66:69], v[230:233], v[234:237]
	v_mfma_f32_16x16x32_f16 v[238:241], v[242:245], v[230:233], v[238:241]
	s_setprio 0
	ds_read_b128 v[70:73], v130 offset:4096
	ds_read_b128 v[242:245], v130 offset:6144
	v_cvt_pk_f16_f32 v9, v12, v13
	v_cvt_pk_f16_f32 v8, v10, v11
	ds_write_b64 v100, v[8:9] offset:53248
	s_add_u32 s0, s22, 0xa0500
	s_addc_u32 s1, s90, 0
	global_load_dwordx4 v[66:69], v201, s[0:1] nt
	s_setprio 1
	s_waitcnt lgkmcnt(1)
	v_mfma_f32_16x16x32_f16 v[26:29], v[70:73], v[218:221], v[26:29]
	v_mfma_f32_16x16x32_f16 v[120:123], v[70:73], v[230:233], v[120:123]
	v_mfma_f32_16x16x32_f16 v[124:127], v[242:245], v[218:221], v[124:127]
	v_mfma_f32_16x16x32_f16 v[146:149], v[242:245], v[222:225], v[146:149]
	v_mfma_f32_16x16x32_f16 v[134:137], v[242:245], v[230:233], v[134:137]
	v_mfma_f32_16x16x32_f16 v[138:141], v[70:73], v[222:225], v[138:141]
	v_mfma_f32_16x16x32_f16 v[142:145], v[70:73], v[226:229], v[142:145]
	v_mfma_f32_16x16x32_f16 v[150:153], v[242:245], v[226:229], v[150:153]
	s_setprio 0
	ds_read_b128 v[8:11], v130 offset:8192
	ds_read_b128 v[242:245], v130 offset:10240
	v_cvt_pk_f16_f32 v13, v36, v37
	v_cvt_pk_f16_f32 v12, v34, v35
	ds_write_b64 v100, v[12:13] offset:57344
	s_add_u32 s0, s22, 0xc0500
	s_addc_u32 s1, s90, 0
	global_load_dwordx4 v[70:73], v201, s[0:1] nt
	s_setprio 1
	s_waitcnt lgkmcnt(1)
	v_mfma_f32_16x16x32_f16 v[22:25], v[8:11], v[218:221], v[22:25]
	v_mfma_f32_16x16x32_f16 v[170:173], v[8:11], v[222:225], v[170:173]
	v_mfma_f32_16x16x32_f16 v[174:177], v[8:11], v[226:229], v[174:177]
	v_mfma_f32_16x16x32_f16 v[162:165], v[8:11], v[230:233], v[162:165]
	v_mfma_f32_16x16x32_f16 v[178:181], v[242:245], v[218:221], v[178:181]
	v_mfma_f32_16x16x32_f16 v[182:185], v[242:245], v[222:225], v[182:185]
	v_mfma_f32_16x16x32_f16 v[186:189], v[242:245], v[226:229], v[186:189]
	v_mfma_f32_16x16x32_f16 v[154:157], v[242:245], v[230:233], v[154:157]
	s_setprio 0
	ds_read_b128 v[8:11], v130 offset:12288
	ds_read_b128 v[242:245], v130 offset:14336
	v_cvt_pk_f16_f32 v13, v40, v41
	v_cvt_pk_f16_f32 v12, v38, v39
	ds_write_b64 v100, v[12:13] offset:61440
	s_add_u32 s0, s22, 0xe0500
	s_addc_u32 s1, s90, 0
	global_load_dwordx4 v[36:39], v201, s[0:1] nt
	s_setprio 1
	s_waitcnt lgkmcnt(1)
	v_mfma_f32_16x16x32_f16 v[246:249], v[8:11], v[218:221], v[18:21]
	v_mfma_f32_16x16x32_f16 v[158:161], v[8:11], v[222:225], v[158:161]
	v_mfma_f32_16x16x32_f16 v[210:213], v[8:11], v[226:229], v[210:213]
	v_mfma_f32_16x16x32_f16 v[166:169], v[8:11], v[230:233], v[166:169]
	v_mfma_f32_16x16x32_f16 v[190:193], v[242:245], v[218:221], v[190:193]
	v_mfma_f32_16x16x32_f16 v[202:205], v[242:245], v[222:225], v[202:205]
	v_mfma_f32_16x16x32_f16 v[206:209], v[242:245], v[226:229], v[206:209]
	v_mfma_f32_16x16x32_f16 v[214:217], v[242:245], v[230:233], v[214:217]
	s_setprio 0
	s_waitcnt vmcnt(6)
	s_waitcnt lgkmcnt(0)
	s_barrier
	ds_read_b128 v[218:221], v131 offset:32768
	ds_read_b128 v[222:225], v131 offset:34816
	ds_read_b128 v[226:229], v131 offset:36864
	ds_read_b128 v[230:233], v131 offset:38912
	ds_read_b128 v[8:11], v129 offset:32768
	ds_read_b128 v[18:21], v129 offset:34816
	s_add_u32 s0, s22, 0x600
	s_addc_u32 s1, s90, 0
	v_lshl_add_u64 v[34:35], s[34:35], 0, v[196:197]
	s_mov_b32 m0, s70
	v_cvt_pk_f16_f32 v3, v2, v3
	global_load_lds_dwordx4 v[34:35], off
	v_cvt_pk_f16_f32 v2, v0, v1
	ds_write_b64 v100, v[2:3]
	global_load_dwordx4 v[0:3], v201, s[0:1] nt
	s_setprio 1
	s_waitcnt lgkmcnt(1)
	v_mfma_f32_16x16x32_f16 v[30:33], v[8:11], v[222:225], v[30:33]
	v_mfma_f32_16x16x32_f16 v[104:107], v[8:11], v[226:229], v[104:107]
	v_mfma_f32_16x16x32_f16 v[108:111], v[18:21], v[218:221], v[108:111]
	v_mfma_f32_16x16x32_f16 v[112:115], v[18:21], v[222:225], v[112:115]
	v_mfma_f32_16x16x32_f16 v[116:119], v[18:21], v[226:229], v[116:119]
	v_mfma_f32_16x16x32_f16 v[242:245], v[8:11], v[218:221], v[14:17]
	v_mfma_f32_16x16x32_f16 v[234:237], v[8:11], v[230:233], v[234:237]
	v_mfma_f32_16x16x32_f16 v[238:241], v[18:21], v[230:233], v[238:241]
	s_setprio 0
	ds_read_b128 v[12:15], v129 offset:36864
	ds_read_b128 v[16:19], v129 offset:38912
	s_mov_b32 m0, s73
	v_lshl_add_u64 v[8:9], v[34:35], 0, s[58:59]
	global_load_lds_dwordx4 v[8:9], off
	v_cvt_pk_f16_f32 v9, v44, v45
	v_cvt_pk_f16_f32 v8, v42, v43
	ds_write_b64 v100, v[8:9] offset:4096
	s_add_u32 s0, s22, 0x20600
	s_addc_u32 s1, s90, 0
	global_load_dwordx4 v[8:11], v201, s[0:1] nt
	s_setprio 1
	s_waitcnt lgkmcnt(1)
	v_mfma_f32_16x16x32_f16 v[40:43], v[12:15], v[218:221], v[26:29]
	v_mfma_f32_16x16x32_f16 v[120:123], v[12:15], v[230:233], v[120:123]
	v_mfma_f32_16x16x32_f16 v[124:127], v[16:19], v[218:221], v[124:127]
	v_mfma_f32_16x16x32_f16 v[146:149], v[16:19], v[222:225], v[146:149]
	v_mfma_f32_16x16x32_f16 v[134:137], v[16:19], v[230:233], v[134:137]
	v_mfma_f32_16x16x32_f16 v[138:141], v[12:15], v[222:225], v[138:141]
	v_mfma_f32_16x16x32_f16 v[142:145], v[12:15], v[226:229], v[142:145]
	v_mfma_f32_16x16x32_f16 v[150:153], v[16:19], v[226:229], v[150:153]
	s_setprio 0
	ds_read_b128 v[16:19], v129 offset:40960
	ds_read_b128 v[26:29], v129 offset:43008
	s_mov_b32 m0, s91
	v_lshl_add_u64 v[12:13], v[34:35], 0, s[60:61]
	global_load_lds_dwordx4 v[12:13], off
	v_lshl_add_u64 v[252:253], v[34:35], 0, s[62:63]
	s_add_u32 m0, m0, 0x2000
	s_nop 0
	global_load_lds_dwordx4 v[252:253], off
	v_cvt_pk_f16_f32 v13, v48, v49
	v_cvt_pk_f16_f32 v12, v46, v47
	ds_write_b64 v100, v[12:13] offset:8192
	s_add_u32 s0, s22, 0x40600
	s_addc_u32 s1, s90, 0
	global_load_dwordx4 v[12:15], v201, s[0:1] nt
	s_setprio 1
	s_waitcnt lgkmcnt(1)
	v_mfma_f32_16x16x32_f16 v[44:47], v[16:19], v[218:221], v[22:25]
	v_mfma_f32_16x16x32_f16 v[170:173], v[16:19], v[222:225], v[170:173]
	v_mfma_f32_16x16x32_f16 v[174:177], v[16:19], v[226:229], v[174:177]
	v_mfma_f32_16x16x32_f16 v[162:165], v[16:19], v[230:233], v[162:165]
	v_mfma_f32_16x16x32_f16 v[178:181], v[26:29], v[218:221], v[178:181]
	v_mfma_f32_16x16x32_f16 v[182:185], v[26:29], v[222:225], v[182:185]
	v_mfma_f32_16x16x32_f16 v[186:189], v[26:29], v[226:229], v[186:189]
	v_mfma_f32_16x16x32_f16 v[154:157], v[26:29], v[230:233], v[154:157]
	s_setprio 0
	ds_read_b128 v[20:23], v129 offset:45056
	ds_read_b128 v[24:27], v129 offset:47104
	v_lshl_add_u64 v[16:17], v[34:35], 0, s[62:63]
	v_cvt_pk_f16_f32 v17, v76, v77
	v_cvt_pk_f16_f32 v16, v74, v75
	ds_write_b64 v100, v[16:17] offset:12288
	s_add_u32 s0, s22, 0x60600
	s_addc_u32 s1, s90, 0
	global_load_dwordx4 v[16:19], v201, s[0:1] nt
	s_setprio 1
	s_waitcnt lgkmcnt(1)
	v_mfma_f32_16x16x32_f16 v[74:77], v[20:23], v[218:221], v[246:249]
	v_mfma_f32_16x16x32_f16 v[158:161], v[20:23], v[222:225], v[158:161]
	v_mfma_f32_16x16x32_f16 v[210:213], v[20:23], v[226:229], v[210:213]
	v_mfma_f32_16x16x32_f16 v[166:169], v[20:23], v[230:233], v[166:169]
	v_mfma_f32_16x16x32_f16 v[190:193], v[24:27], v[218:221], v[190:193]
	v_mfma_f32_16x16x32_f16 v[202:205], v[24:27], v[222:225], v[202:205]
	v_mfma_f32_16x16x32_f16 v[206:209], v[24:27], v[226:229], v[206:209]
	v_mfma_f32_16x16x32_f16 v[214:217], v[24:27], v[230:233], v[214:217]
	s_setprio 0
	ds_read_b128 v[218:221], v128 offset:32768
	ds_read_b128 v[222:225], v128 offset:34816
	ds_read_b128 v[226:229], v128 offset:36864
	ds_read_b128 v[230:233], v128 offset:38912
	ds_read_b128 v[24:27], v130 offset:32768
	ds_read_b128 v[246:249], v130 offset:34816
	v_cvt_pk_f16_f32 v21, v80, v81
	v_cvt_pk_f16_f32 v20, v78, v79
	ds_write_b64 v100, v[20:21] offset:16384
	s_add_u32 s0, s22, 0x80600
	s_addc_u32 s1, s90, 0
	global_load_dwordx4 v[20:23], v201, s[0:1] nt
	s_setprio 1
	s_waitcnt lgkmcnt(1)
	v_mfma_f32_16x16x32_f16 v[78:81], v[24:27], v[218:221], v[242:245]
	v_mfma_f32_16x16x32_f16 v[104:107], v[24:27], v[226:229], v[104:107]
	v_mfma_f32_16x16x32_f16 v[108:111], v[246:249], v[218:221], v[108:111]
	v_mfma_f32_16x16x32_f16 v[112:115], v[246:249], v[222:225], v[112:115]
	v_mfma_f32_16x16x32_f16 v[116:119], v[246:249], v[226:229], v[116:119]
	v_mfma_f32_16x16x32_f16 v[242:245], v[24:27], v[222:225], v[30:33]
	v_mfma_f32_16x16x32_f16 v[234:237], v[24:27], v[230:233], v[234:237]
	v_mfma_f32_16x16x32_f16 v[238:241], v[246:249], v[230:233], v[238:241]
	s_setprio 0
	ds_read_b128 v[28:31], v130 offset:36864
	ds_read_b128 v[32:35], v130 offset:38912
	v_cvt_pk_f16_f32 v25, v84, v85
	v_cvt_pk_f16_f32 v24, v82, v83
	ds_write_b64 v100, v[24:25] offset:20480
	s_add_u32 s0, s22, 0xa0600
	s_addc_u32 s1, s90, 0
	global_load_dwordx4 v[24:27], v201, s[0:1] nt
	s_setprio 1
	s_waitcnt lgkmcnt(1)
	v_mfma_f32_16x16x32_f16 v[82:85], v[28:31], v[218:221], v[40:43]
	v_mfma_f32_16x16x32_f16 v[120:123], v[28:31], v[230:233], v[120:123]
	v_mfma_f32_16x16x32_f16 v[124:127], v[32:35], v[218:221], v[124:127]
	v_mfma_f32_16x16x32_f16 v[146:149], v[32:35], v[222:225], v[146:149]
	v_mfma_f32_16x16x32_f16 v[134:137], v[32:35], v[230:233], v[134:137]
	v_mfma_f32_16x16x32_f16 v[138:141], v[28:31], v[222:225], v[138:141]
	v_mfma_f32_16x16x32_f16 v[142:145], v[28:31], v[226:229], v[142:145]
	v_mfma_f32_16x16x32_f16 v[150:153], v[32:35], v[226:229], v[150:153]
	s_setprio 0
	ds_read_b128 v[32:35], v130 offset:40960
	ds_read_b128 v[40:43], v130 offset:43008
	v_cvt_pk_f16_f32 v29, v88, v89
	v_cvt_pk_f16_f32 v28, v86, v87
	ds_write_b64 v100, v[28:29] offset:24576
	s_add_u32 s0, s22, 0xc0600
	s_addc_u32 s1, s90, 0
	global_load_dwordx4 v[28:31], v201, s[0:1] nt
	s_setprio 1
	s_waitcnt lgkmcnt(1)
	v_mfma_f32_16x16x32_f16 v[86:89], v[32:35], v[218:221], v[44:47]
	v_mfma_f32_16x16x32_f16 v[170:173], v[32:35], v[222:225], v[170:173]
	v_mfma_f32_16x16x32_f16 v[174:177], v[32:35], v[226:229], v[174:177]
	v_mfma_f32_16x16x32_f16 v[162:165], v[32:35], v[230:233], v[162:165]
	v_mfma_f32_16x16x32_f16 v[178:181], v[40:43], v[218:221], v[178:181]
	v_mfma_f32_16x16x32_f16 v[182:185], v[40:43], v[222:225], v[182:185]
	v_mfma_f32_16x16x32_f16 v[186:189], v[40:43], v[226:229], v[186:189]
	v_mfma_f32_16x16x32_f16 v[154:157], v[40:43], v[230:233], v[154:157]
	s_setprio 0
	ds_read_b128 v[40:43], v130 offset:45056
	ds_read_b128 v[44:47], v130 offset:47104
	v_cvt_pk_f16_f32 v33, v92, v93
	v_cvt_pk_f16_f32 v32, v90, v91
	ds_write_b64 v100, v[32:33] offset:28672
	s_add_u32 s0, s22, 0xe0600
	s_addc_u32 s1, s90, 0
	global_load_dwordx4 v[32:35], v201, s[0:1] nt
	s_setprio 1
	s_waitcnt lgkmcnt(1)
	v_mfma_f32_16x16x32_f16 v[74:77], v[40:43], v[218:221], v[74:77]
	v_mfma_f32_16x16x32_f16 v[90:93], v[40:43], v[222:225], v[158:161]
	v_mfma_f32_16x16x32_f16 v[158:161], v[40:43], v[226:229], v[210:213]
	v_mfma_f32_16x16x32_f16 v[166:169], v[40:43], v[230:233], v[166:169]
	v_mfma_f32_16x16x32_f16 v[190:193], v[44:47], v[218:221], v[190:193]
	v_mfma_f32_16x16x32_f16 v[202:205], v[44:47], v[222:225], v[202:205]
	v_mfma_f32_16x16x32_f16 v[206:209], v[44:47], v[226:229], v[206:209]
	v_mfma_f32_16x16x32_f16 v[210:213], v[44:47], v[230:233], v[214:217]
	s_setprio 0
	s_waitcnt vmcnt(6)
	s_waitcnt lgkmcnt(0)
	s_barrier
	s_nop 0
	ds_read_b128 v[214:217], v131
	ds_read_b128 v[218:221], v131 offset:2048
	ds_read_b128 v[222:225], v131 offset:4096
	ds_read_b128 v[226:229], v131 offset:6144
	ds_read_b128 v[40:43], v129
	ds_read_b128 v[44:47], v129 offset:2048
	s_add_u32 s70, s22, 0x700
	s_addc_u32 s71, s90, 0
	v_lshl_add_u64 v[198:199], s[36:37], 0, v[196:197]
	v_readfirstlane_b32 s0, v95
	s_mov_b32 m0, s0
	v_cvt_pk_f16_f32 v7, v6, v7
	global_load_lds_dwordx4 v[198:199], off
	v_cvt_pk_f16_f32 v6, v4, v5
	ds_write_b64 v100, v[6:7] offset:32768
	global_load_dwordx4 v[4:7], v201, s[70:71] nt
	s_setprio 1
	s_waitcnt lgkmcnt(1)
	v_mfma_f32_16x16x32_f16 v[78:81], v[40:43], v[214:217], v[78:81]
	v_mfma_f32_16x16x32_f16 v[104:107], v[40:43], v[222:225], v[104:107]
	v_mfma_f32_16x16x32_f16 v[108:111], v[44:47], v[214:217], v[108:111]
	v_mfma_f32_16x16x32_f16 v[112:115], v[44:47], v[218:221], v[112:115]
	v_mfma_f32_16x16x32_f16 v[116:119], v[44:47], v[222:225], v[116:119]
	v_mfma_f32_16x16x32_f16 v[230:233], v[40:43], v[218:221], v[242:245]
	v_mfma_f32_16x16x32_f16 v[234:237], v[40:43], v[226:229], v[234:237]
	v_mfma_f32_16x16x32_f16 v[238:241], v[44:47], v[226:229], v[238:241]
	s_setprio 0
	ds_read_b128 v[44:47], v129 offset:4096
	ds_read_b128 v[242:245], v129 offset:6144
	v_readfirstlane_b32 s72, v96
	v_lshl_add_u64 v[40:41], v[198:199], 0, s[58:59]
	s_mov_b32 m0, s72
	s_nop 0
	global_load_lds_dwordx4 v[40:41], off
	v_cvt_pk_f16_f32 v41, v52, v53
	v_cvt_pk_f16_f32 v40, v50, v51
	ds_write_b64 v100, v[40:41] offset:36864
	s_add_u32 s70, s22, 0x20700
	s_addc_u32 s71, s90, 0
	global_load_dwordx4 v[40:43], v201, s[70:71] nt
	s_setprio 1
	s_waitcnt lgkmcnt(1)
	v_mfma_f32_16x16x32_f16 v[82:85], v[44:47], v[214:217], v[82:85]
	v_mfma_f32_16x16x32_f16 v[120:123], v[44:47], v[226:229], v[120:123]
	v_mfma_f32_16x16x32_f16 v[124:127], v[242:245], v[214:217], v[124:127]
	v_mfma_f32_16x16x32_f16 v[146:149], v[242:245], v[218:221], v[146:149]
	v_mfma_f32_16x16x32_f16 v[134:137], v[242:245], v[226:229], v[134:137]
	v_mfma_f32_16x16x32_f16 v[138:141], v[44:47], v[218:221], v[138:141]
	v_mfma_f32_16x16x32_f16 v[142:145], v[44:47], v[222:225], v[142:145]
	v_mfma_f32_16x16x32_f16 v[150:153], v[242:245], v[222:225], v[150:153]
	s_setprio 0
	ds_read_b128 v[48:51], v129 offset:8192
	ds_read_b128 v[242:245], v129 offset:10240
	v_readfirstlane_b32 s71, v97
	v_lshl_add_u64 v[44:45], v[198:199], 0, s[60:61]
	s_mov_b32 m0, s71
	s_nop 0
	global_load_lds_dwordx4 v[44:45], off
	v_lshl_add_u64 v[252:253], v[198:199], 0, s[62:63]
	s_add_u32 m0, m0, 0x2000
	s_nop 0
	global_load_lds_dwordx4 v[252:253], off
	v_cvt_pk_f16_f32 v45, v56, v57
	v_cvt_pk_f16_f32 v44, v54, v55
	ds_write_b64 v100, v[44:45] offset:40960
	s_add_u32 s80, s22, 0x40700
	s_addc_u32 s81, s90, 0
	global_load_dwordx4 v[44:47], v201, s[80:81] nt
	s_setprio 1
	s_waitcnt lgkmcnt(1)
	v_mfma_f32_16x16x32_f16 v[86:89], v[48:51], v[214:217], v[86:89]
	v_mfma_f32_16x16x32_f16 v[170:173], v[48:51], v[218:221], v[170:173]
	v_mfma_f32_16x16x32_f16 v[174:177], v[48:51], v[222:225], v[174:177]
	v_mfma_f32_16x16x32_f16 v[162:165], v[48:51], v[226:229], v[162:165]
	v_mfma_f32_16x16x32_f16 v[178:181], v[242:245], v[214:217], v[178:181]
	v_mfma_f32_16x16x32_f16 v[182:185], v[242:245], v[218:221], v[182:185]
	v_mfma_f32_16x16x32_f16 v[186:189], v[242:245], v[222:225], v[186:189]
	v_mfma_f32_16x16x32_f16 v[154:157], v[242:245], v[226:229], v[154:157]
	s_setprio 0
	ds_read_b128 v[52:55], v129 offset:12288
	ds_read_b128 v[242:245], v129 offset:14336
	v_readfirstlane_b32 s70, v98
	v_lshl_add_u64 v[48:49], v[198:199], 0, s[62:63]
	v_cvt_pk_f16_f32 v49, v60, v61
	v_cvt_pk_f16_f32 v48, v58, v59
	ds_write_b64 v100, v[48:49] offset:45056
	s_add_u32 s80, s22, 0x60700
	s_addc_u32 s81, s90, 0
	global_load_dwordx4 v[48:51], v201, s[80:81] nt
	s_setprio 1
	s_waitcnt lgkmcnt(1)
	v_mfma_f32_16x16x32_f16 v[74:77], v[52:55], v[214:217], v[74:77]
	v_mfma_f32_16x16x32_f16 v[90:93], v[52:55], v[218:221], v[90:93]
	v_mfma_f32_16x16x32_f16 v[158:161], v[52:55], v[222:225], v[158:161]
	v_mfma_f32_16x16x32_f16 v[166:169], v[52:55], v[226:229], v[166:169]
	v_mfma_f32_16x16x32_f16 v[190:193], v[242:245], v[214:217], v[190:193]
	v_mfma_f32_16x16x32_f16 v[202:205], v[242:245], v[218:221], v[202:205]
	v_mfma_f32_16x16x32_f16 v[206:209], v[242:245], v[222:225], v[206:209]
	v_mfma_f32_16x16x32_f16 v[210:213], v[242:245], v[226:229], v[210:213]
	s_setprio 0
	ds_read_b128 v[214:217], v128
	ds_read_b128 v[218:221], v128 offset:2048
	ds_read_b128 v[222:225], v128 offset:4096
	ds_read_b128 v[226:229], v128 offset:6144
	ds_read_b128 v[56:59], v130
	ds_read_b128 v[242:245], v130 offset:2048
	v_cvt_pk_f16_f32 v53, v64, v65
	v_cvt_pk_f16_f32 v52, v62, v63
	ds_write_b64 v100, v[52:53] offset:49152
	s_add_u32 s80, s22, 0x80700
	s_addc_u32 s81, s90, 0
	global_load_dwordx4 v[52:55], v201, s[80:81] nt
	s_setprio 1
	s_waitcnt lgkmcnt(1)
	v_mfma_f32_16x16x32_f16 v[78:81], v[56:59], v[214:217], v[78:81]
	v_mfma_f32_16x16x32_f16 v[104:107], v[56:59], v[222:225], v[104:107]
	v_mfma_f32_16x16x32_f16 v[108:111], v[242:245], v[214:217], v[108:111]
	v_mfma_f32_16x16x32_f16 v[112:115], v[242:245], v[218:221], v[112:115]
	v_mfma_f32_16x16x32_f16 v[116:119], v[242:245], v[222:225], v[116:119]
	v_mfma_f32_16x16x32_f16 v[230:233], v[56:59], v[218:221], v[230:233]
	v_mfma_f32_16x16x32_f16 v[234:237], v[56:59], v[226:229], v[234:237]
	v_mfma_f32_16x16x32_f16 v[238:241], v[242:245], v[226:229], v[238:241]
	s_setprio 0
	ds_read_b128 v[60:63], v130 offset:4096
	ds_read_b128 v[242:245], v130 offset:6144
	v_cvt_pk_f16_f32 v57, v68, v69
	v_cvt_pk_f16_f32 v56, v66, v67
	ds_write_b64 v100, v[56:57] offset:53248
	s_add_u32 s80, s22, 0xa0700
	s_addc_u32 s81, s90, 0
	global_load_dwordx4 v[56:59], v201, s[80:81] nt
	s_setprio 1
	s_waitcnt lgkmcnt(1)
	v_mfma_f32_16x16x32_f16 v[82:85], v[60:63], v[214:217], v[82:85]
	v_mfma_f32_16x16x32_f16 v[120:123], v[60:63], v[226:229], v[120:123]
	v_mfma_f32_16x16x32_f16 v[124:127], v[242:245], v[214:217], v[124:127]
	v_mfma_f32_16x16x32_f16 v[146:149], v[242:245], v[218:221], v[146:149]
	v_mfma_f32_16x16x32_f16 v[134:137], v[242:245], v[226:229], v[134:137]
	v_mfma_f32_16x16x32_f16 v[138:141], v[60:63], v[218:221], v[138:141]
	v_mfma_f32_16x16x32_f16 v[142:145], v[60:63], v[222:225], v[142:145]
	v_mfma_f32_16x16x32_f16 v[150:153], v[242:245], v[222:225], v[150:153]
	s_setprio 0
	ds_read_b128 v[64:67], v130 offset:8192
	ds_read_b128 v[242:245], v130 offset:10240
	v_cvt_pk_f16_f32 v61, v72, v73
	v_cvt_pk_f16_f32 v60, v70, v71
	ds_write_b64 v100, v[60:61] offset:57344
	s_add_u32 s80, s22, 0xc0700
	s_addc_u32 s81, s90, 0
	global_load_dwordx4 v[60:63], v201, s[80:81] nt
	s_setprio 1
	s_waitcnt lgkmcnt(1)
	v_mfma_f32_16x16x32_f16 v[86:89], v[64:67], v[214:217], v[86:89]
	v_mfma_f32_16x16x32_f16 v[170:173], v[64:67], v[218:221], v[170:173]
	v_mfma_f32_16x16x32_f16 v[174:177], v[64:67], v[222:225], v[174:177]
	v_mfma_f32_16x16x32_f16 v[162:165], v[64:67], v[226:229], v[162:165]
	v_mfma_f32_16x16x32_f16 v[178:181], v[242:245], v[214:217], v[178:181]
	v_mfma_f32_16x16x32_f16 v[182:185], v[242:245], v[218:221], v[182:185]
	v_mfma_f32_16x16x32_f16 v[186:189], v[242:245], v[222:225], v[186:189]
	v_mfma_f32_16x16x32_f16 v[154:157], v[242:245], v[226:229], v[154:157]
	s_setprio 0
	ds_read_b128 v[64:67], v130 offset:12288
	ds_read_b128 v[68:71], v130 offset:14336
	v_cvt_pk_f16_f32 v39, v38, v39
	v_cvt_pk_f16_f32 v38, v36, v37
	ds_write_b64 v100, v[38:39] offset:61440
	s_add_u32 s80, s22, 0xe0700
	s_addc_u32 s81, s90, 0
	global_load_dwordx4 v[36:39], v201, s[80:81] nt
	s_setprio 1
	s_waitcnt lgkmcnt(1)
	v_mfma_f32_16x16x32_f16 v[90:93], v[64:67], v[218:221], v[90:93]
	v_mfma_f32_16x16x32_f16 v[242:245], v[64:67], v[214:217], v[74:77]
	v_mfma_f32_16x16x32_f16 v[158:161], v[64:67], v[222:225], v[158:161]
	v_mfma_f32_16x16x32_f16 v[166:169], v[64:67], v[226:229], v[166:169]
	v_mfma_f32_16x16x32_f16 v[190:193], v[68:71], v[214:217], v[190:193]
	v_mfma_f32_16x16x32_f16 v[202:205], v[68:71], v[218:221], v[202:205]
	v_mfma_f32_16x16x32_f16 v[206:209], v[68:71], v[222:225], v[206:209]
	v_mfma_f32_16x16x32_f16 v[210:213], v[68:71], v[226:229], v[210:213]
	s_setprio 0
	s_waitcnt vmcnt(6)
	s_waitcnt lgkmcnt(0)
	s_barrier
	ds_read_b128 v[214:217], v131 offset:32768
	ds_read_b128 v[218:221], v131 offset:34816
	ds_read_b128 v[222:225], v131 offset:36864
	ds_read_b128 v[226:229], v131 offset:38912
	ds_read_b128 v[64:67], v129 offset:32768
	ds_read_b128 v[68:71], v129 offset:34816
	s_add_u32 s80, s22, 0x800
	s_addc_u32 s81, s90, 0
	v_lshl_add_u64 v[198:199], s[38:39], 0, v[196:197]
	v_readfirstlane_b32 s1, v94
	s_mov_b32 m0, s1
	v_cvt_pk_f16_f32 v3, v2, v3
	global_load_lds_dwordx4 v[198:199], off
	v_cvt_pk_f16_f32 v2, v0, v1
	ds_write_b64 v100, v[2:3]
	global_load_dwordx4 v[0:3], v201, s[80:81] nt
	s_setprio 1
	s_waitcnt lgkmcnt(1)
	v_mfma_f32_16x16x32_f16 v[104:107], v[64:67], v[222:225], v[104:107]
	v_mfma_f32_16x16x32_f16 v[108:111], v[68:71], v[214:217], v[108:111]
	v_mfma_f32_16x16x32_f16 v[112:115], v[68:71], v[218:221], v[112:115]
	v_mfma_f32_16x16x32_f16 v[116:119], v[68:71], v[222:225], v[116:119]
	v_mfma_f32_16x16x32_f16 v[246:249], v[64:67], v[214:217], v[78:81]
	v_mfma_f32_16x16x32_f16 v[230:233], v[64:67], v[218:221], v[230:233]
	v_mfma_f32_16x16x32_f16 v[234:237], v[64:67], v[226:229], v[234:237]
	v_mfma_f32_16x16x32_f16 v[238:241], v[68:71], v[226:229], v[238:241]
	s_setprio 0
	ds_read_b128 v[68:71], v129 offset:36864
	ds_read_b128 v[72:75], v129 offset:38912
	v_readfirstlane_b32 s92, v99
	v_lshl_add_u64 v[64:65], v[198:199], 0, s[58:59]
	s_mov_b32 m0, s92
	v_cvt_pk_f16_f32 v11, v10, v11
	global_load_lds_dwordx4 v[64:65], off
	v_cvt_pk_f16_f32 v10, v8, v9
	ds_write_b64 v100, v[10:11] offset:4096
	s_add_u32 s80, s22, 0x20800
	s_addc_u32 s81, s90, 0
	global_load_dwordx4 v[64:67], v201, s[80:81] nt
	s_setprio 1
	s_waitcnt lgkmcnt(1)
	v_mfma_f32_16x16x32_f16 v[8:11], v[68:71], v[214:217], v[82:85]
	v_mfma_f32_16x16x32_f16 v[120:123], v[68:71], v[226:229], v[120:123]
	v_mfma_f32_16x16x32_f16 v[124:127], v[72:75], v[214:217], v[124:127]
	v_mfma_f32_16x16x32_f16 v[146:149], v[72:75], v[218:221], v[146:149]
	v_mfma_f32_16x16x32_f16 v[134:137], v[72:75], v[226:229], v[134:137]
	v_mfma_f32_16x16x32_f16 v[138:141], v[68:71], v[218:221], v[138:141]
	v_mfma_f32_16x16x32_f16 v[142:145], v[68:71], v[222:225], v[142:145]
	v_mfma_f32_16x16x32_f16 v[150:153], v[72:75], v[222:225], v[150:153]
	s_setprio 0
	ds_read_b128 v[72:75], v129 offset:40960
	ds_read_b128 v[76:79], v129 offset:43008
	v_readfirstlane_b32 s91, v101
	v_lshl_add_u64 v[68:69], v[198:199], 0, s[60:61]
	s_mov_b32 m0, s91
	v_cvt_pk_f16_f32 v15, v14, v15
	global_load_lds_dwordx4 v[68:69], off
	v_lshl_add_u64 v[252:253], v[198:199], 0, s[62:63]
	s_add_u32 m0, m0, 0x2000
	s_nop 0
	global_load_lds_dwordx4 v[252:253], off
	v_cvt_pk_f16_f32 v14, v12, v13
	ds_write_b64 v100, v[14:15] offset:8192
	s_add_u32 s80, s22, 0x40800
	s_addc_u32 s81, s90, 0
	global_load_dwordx4 v[68:71], v201, s[80:81] nt
	s_setprio 1
	s_waitcnt lgkmcnt(1)
	v_mfma_f32_16x16x32_f16 v[12:15], v[72:75], v[214:217], v[86:89]
	v_mfma_f32_16x16x32_f16 v[170:173], v[72:75], v[218:221], v[170:173]
	v_mfma_f32_16x16x32_f16 v[174:177], v[72:75], v[222:225], v[174:177]
	v_mfma_f32_16x16x32_f16 v[162:165], v[72:75], v[226:229], v[162:165]
	v_mfma_f32_16x16x32_f16 v[178:181], v[76:79], v[214:217], v[178:181]
	v_mfma_f32_16x16x32_f16 v[182:185], v[76:79], v[218:221], v[182:185]
	v_mfma_f32_16x16x32_f16 v[186:189], v[76:79], v[222:225], v[186:189]
	v_mfma_f32_16x16x32_f16 v[154:157], v[76:79], v[226:229], v[154:157]
	s_setprio 0
	ds_read_b128 v[76:79], v129 offset:45056
	ds_read_b128 v[80:83], v129 offset:47104
	v_readfirstlane_b32 s73, v102
	v_lshl_add_u64 v[72:73], v[198:199], 0, s[62:63]
	v_cvt_pk_f16_f32 v19, v18, v19
	v_cvt_pk_f16_f32 v18, v16, v17
	ds_write_b64 v100, v[18:19] offset:12288
	s_add_u32 s80, s22, 0x60800
	s_addc_u32 s81, s90, 0
	global_load_dwordx4 v[72:75], v201, s[80:81] nt
	s_setprio 1
	s_waitcnt lgkmcnt(1)
	v_mfma_f32_16x16x32_f16 v[16:19], v[76:79], v[214:217], v[242:245]
	v_mfma_f32_16x16x32_f16 v[242:245], v[76:79], v[218:221], v[90:93]
	v_mfma_f32_16x16x32_f16 v[158:161], v[76:79], v[222:225], v[158:161]
	v_mfma_f32_16x16x32_f16 v[166:169], v[76:79], v[226:229], v[166:169]
	v_mfma_f32_16x16x32_f16 v[190:193], v[80:83], v[214:217], v[190:193]
	v_mfma_f32_16x16x32_f16 v[202:205], v[80:83], v[218:221], v[202:205]
	v_mfma_f32_16x16x32_f16 v[206:209], v[80:83], v[222:225], v[206:209]
	v_mfma_f32_16x16x32_f16 v[210:213], v[80:83], v[226:229], v[210:213]
	s_setprio 0
	ds_read_b128 v[214:217], v128 offset:32768
	ds_read_b128 v[218:221], v128 offset:34816
	ds_read_b128 v[222:225], v128 offset:36864
	ds_read_b128 v[226:229], v128 offset:38912
	ds_read_b128 v[80:83], v130 offset:32768
	ds_read_b128 v[84:87], v130 offset:34816
	v_cvt_pk_f16_f32 v23, v22, v23
	v_cvt_pk_f16_f32 v22, v20, v21
	ds_write_b64 v100, v[22:23] offset:16384
	s_add_u32 s80, s22, 0x80800
	s_addc_u32 s81, s90, 0
	global_load_dwordx4 v[76:79], v201, s[80:81] nt
	s_setprio 1
	s_waitcnt lgkmcnt(1)
	v_mfma_f32_16x16x32_f16 v[20:23], v[80:83], v[214:217], v[246:249]
	v_mfma_f32_16x16x32_f16 v[104:107], v[80:83], v[222:225], v[104:107]
	v_mfma_f32_16x16x32_f16 v[108:111], v[84:87], v[214:217], v[108:111]
	v_mfma_f32_16x16x32_f16 v[112:115], v[84:87], v[218:221], v[112:115]
	v_mfma_f32_16x16x32_f16 v[116:119], v[84:87], v[222:225], v[116:119]
	v_mfma_f32_16x16x32_f16 v[230:233], v[80:83], v[218:221], v[230:233]
	v_mfma_f32_16x16x32_f16 v[234:237], v[80:83], v[226:229], v[234:237]
	v_mfma_f32_16x16x32_f16 v[238:241], v[84:87], v[226:229], v[238:241]
	s_setprio 0
	ds_read_b128 v[84:87], v130 offset:36864
	ds_read_b128 v[88:91], v130 offset:38912
	v_cvt_pk_f16_f32 v27, v26, v27
	v_cvt_pk_f16_f32 v26, v24, v25
	ds_write_b64 v100, v[26:27] offset:20480
	s_add_u32 s80, s22, 0xa0800
	s_addc_u32 s81, s90, 0
	global_load_dwordx4 v[80:83], v201, s[80:81] nt
	s_setprio 1
	s_waitcnt lgkmcnt(1)
	v_mfma_f32_16x16x32_f16 v[24:27], v[84:87], v[214:217], v[8:11]
	v_mfma_f32_16x16x32_f16 v[120:123], v[84:87], v[226:229], v[120:123]
	v_mfma_f32_16x16x32_f16 v[124:127], v[88:91], v[214:217], v[124:127]
	v_mfma_f32_16x16x32_f16 v[146:149], v[88:91], v[218:221], v[146:149]
	v_mfma_f32_16x16x32_f16 v[134:137], v[88:91], v[226:229], v[134:137]
	v_mfma_f32_16x16x32_f16 v[138:141], v[84:87], v[218:221], v[138:141]
	v_mfma_f32_16x16x32_f16 v[142:145], v[84:87], v[222:225], v[142:145]
	v_mfma_f32_16x16x32_f16 v[150:153], v[88:91], v[222:225], v[150:153]
	s_setprio 0
	ds_read_b128 v[8:11], v130 offset:40960
	ds_read_b128 v[88:91], v130 offset:43008
	v_cvt_pk_f16_f32 v31, v30, v31
	v_cvt_pk_f16_f32 v30, v28, v29
	ds_write_b64 v100, v[30:31] offset:24576
	s_add_u32 s80, s22, 0xc0800
	s_addc_u32 s81, s90, 0
	global_load_dwordx4 v[84:87], v201, s[80:81] nt
	s_setprio 1
	s_waitcnt lgkmcnt(1)
	v_mfma_f32_16x16x32_f16 v[12:15], v[8:11], v[214:217], v[12:15]
	v_mfma_f32_16x16x32_f16 v[28:31], v[8:11], v[218:221], v[170:173]
	v_mfma_f32_16x16x32_f16 v[170:173], v[8:11], v[222:225], v[174:177]
	v_mfma_f32_16x16x32_f16 v[162:165], v[8:11], v[226:229], v[162:165]
	v_mfma_f32_16x16x32_f16 v[174:177], v[88:91], v[214:217], v[178:181]
	v_mfma_f32_16x16x32_f16 v[178:181], v[88:91], v[218:221], v[182:185]
	v_mfma_f32_16x16x32_f16 v[182:185], v[88:91], v[222:225], v[186:189]
	v_mfma_f32_16x16x32_f16 v[154:157], v[88:91], v[226:229], v[154:157]
	s_setprio 0
	ds_read_b128 v[8:11], v130 offset:45056
	ds_read_b128 v[186:189], v130 offset:47104
	v_cvt_pk_f16_f32 v35, v34, v35
	v_cvt_pk_f16_f32 v34, v32, v33
	ds_write_b64 v100, v[34:35] offset:28672
	s_add_u32 s80, s22, 0xe0800
	s_addc_u32 s81, s90, 0
	global_load_dwordx4 v[88:91], v201, s[80:81] nt
	s_setprio 1
	s_waitcnt lgkmcnt(1)
	v_mfma_f32_16x16x32_f16 v[16:19], v[8:11], v[214:217], v[16:19]
	v_mfma_f32_16x16x32_f16 v[32:35], v[8:11], v[218:221], v[242:245]
	v_mfma_f32_16x16x32_f16 v[158:161], v[8:11], v[222:225], v[158:161]
	v_mfma_f32_16x16x32_f16 v[166:169], v[8:11], v[226:229], v[166:169]
	v_mfma_f32_16x16x32_f16 v[190:193], v[186:189], v[214:217], v[190:193]
	v_mfma_f32_16x16x32_f16 v[202:205], v[186:189], v[218:221], v[202:205]
	v_mfma_f32_16x16x32_f16 v[206:209], v[186:189], v[222:225], v[206:209]
	v_mfma_f32_16x16x32_f16 v[186:189], v[186:189], v[226:229], v[210:213]
	s_setprio 0
	s_waitcnt vmcnt(6)
	s_waitcnt lgkmcnt(0)
	s_barrier
	s_nop 0
	ds_read_b128 v[210:213], v131
	ds_read_b128 v[214:217], v131 offset:2048
	ds_read_b128 v[218:221], v131 offset:4096
	ds_read_b128 v[222:225], v131 offset:6144
	ds_read_b128 v[8:11], v129
	ds_read_b128 v[226:229], v129 offset:2048
	s_add_u32 s80, s22, 0x900
	v_lshl_add_u64 v[92:93], s[40:41], 0, v[196:197]
	s_addc_u32 s81, s90, 0
	v_cvt_pk_f16_f32 v7, v6, v7
	s_cmp_lg_u32 s2, 0
	s_cbranch_scc1 .Lres_skip_0
	s_add_u32 m0, s0, 0x18000
	s_nop 0
	global_load_lds_dwordx4 v[92:93], off

.Lres_skip_3:
	v_cvt_pk_f16_f32 v45, v50, v51
	v_cvt_pk_f16_f32 v44, v48, v49
	ds_write_b64 v100, v[44:45] offset:45056
	s_add_u32 s70, s22, 0x60900
	s_addc_u32 s71, s90, 0
	global_load_dwordx4 v[44:47], v201, s[70:71] nt
	s_setprio 1
	s_waitcnt lgkmcnt(1)
	v_mfma_f32_16x16x32_f16 v[16:19], v[238:241], v[210:213], v[16:19]
	v_mfma_f32_16x16x32_f16 v[32:35], v[238:241], v[214:217], v[32:35]
	v_mfma_f32_16x16x32_f16 v[158:161], v[238:241], v[218:221], v[158:161]
	v_mfma_f32_16x16x32_f16 v[166:169], v[238:241], v[222:225], v[166:169]
	v_mfma_f32_16x16x32_f16 v[190:193], v[242:245], v[210:213], v[190:193]
	v_mfma_f32_16x16x32_f16 v[202:205], v[242:245], v[214:217], v[202:205]
	v_mfma_f32_16x16x32_f16 v[206:209], v[242:245], v[218:221], v[206:209]
	v_mfma_f32_16x16x32_f16 v[186:189], v[242:245], v[222:225], v[186:189]
	s_setprio 0
	ds_read_b128 v[210:213], v128
	ds_read_b128 v[214:217], v128 offset:2048
	ds_read_b128 v[218:221], v128 offset:4096
	ds_read_b128 v[222:225], v128 offset:6144
	ds_read_b128 v[238:241], v130
	ds_read_b128 v[242:245], v130 offset:2048
	v_cvt_pk_f16_f32 v49, v54, v55
	v_cvt_pk_f16_f32 v48, v52, v53
	ds_write_b64 v100, v[48:49] offset:49152
	s_add_u32 s70, s22, 0x80900
	s_addc_u32 s71, s90, 0
	global_load_dwordx4 v[48:51], v201, s[70:71] nt
	s_setprio 1
	s_waitcnt lgkmcnt(1)
	v_mfma_f32_16x16x32_f16 v[20:23], v[238:241], v[210:213], v[20:23]
	v_mfma_f32_16x16x32_f16 v[104:107], v[238:241], v[218:221], v[104:107]
	v_mfma_f32_16x16x32_f16 v[108:111], v[242:245], v[210:213], v[108:111]
	v_mfma_f32_16x16x32_f16 v[112:115], v[242:245], v[214:217], v[112:115]
	v_mfma_f32_16x16x32_f16 v[116:119], v[242:245], v[218:221], v[116:119]
	v_mfma_f32_16x16x32_f16 v[230:233], v[238:241], v[214:217], v[230:233]
	v_mfma_f32_16x16x32_f16 v[234:237], v[238:241], v[222:225], v[234:237]
	v_mfma_f32_16x16x32_f16 v[226:229], v[242:245], v[222:225], v[226:229]
	s_setprio 0
	ds_read_b128 v[238:241], v130 offset:4096
	ds_read_b128 v[242:245], v130 offset:6144
	v_cvt_pk_f16_f32 v53, v58, v59
	v_cvt_pk_f16_f32 v52, v56, v57
	ds_write_b64 v100, v[52:53] offset:53248
	s_add_u32 s70, s22, 0xa0900
	s_addc_u32 s71, s90, 0
	global_load_dwordx4 v[52:55], v201, s[70:71] nt
	s_setprio 1
	s_waitcnt lgkmcnt(1)
	v_mfma_f32_16x16x32_f16 v[24:27], v[238:241], v[210:213], v[24:27]
	v_mfma_f32_16x16x32_f16 v[120:123], v[238:241], v[222:225], v[120:123]
	v_mfma_f32_16x16x32_f16 v[124:127], v[242:245], v[210:213], v[124:127]
	v_mfma_f32_16x16x32_f16 v[146:149], v[242:245], v[214:217], v[146:149]
	v_mfma_f32_16x16x32_f16 v[134:137], v[242:245], v[222:225], v[134:137]
	v_mfma_f32_16x16x32_f16 v[138:141], v[238:241], v[214:217], v[138:141]
	v_mfma_f32_16x16x32_f16 v[142:145], v[238:241], v[218:221], v[142:145]
	v_mfma_f32_16x16x32_f16 v[150:153], v[242:245], v[218:221], v[150:153]
	s_setprio 0
	ds_read_b128 v[238:241], v130 offset:8192
	ds_read_b128 v[242:245], v130 offset:10240
	v_cvt_pk_f16_f32 v57, v62, v63
	v_cvt_pk_f16_f32 v56, v60, v61
	ds_write_b64 v100, v[56:57] offset:57344
	s_add_u32 s70, s22, 0xc0900
	s_addc_u32 s71, s90, 0
	global_load_dwordx4 v[56:59], v201, s[70:71] nt
	s_setprio 1
	s_waitcnt lgkmcnt(1)
	v_mfma_f32_16x16x32_f16 v[28:31], v[238:241], v[214:217], v[28:31]
	v_mfma_f32_16x16x32_f16 v[246:249], v[238:241], v[210:213], v[12:15]
	v_mfma_f32_16x16x32_f16 v[170:173], v[238:241], v[218:221], v[170:173]
	v_mfma_f32_16x16x32_f16 v[162:165], v[238:241], v[222:225], v[162:165]
	v_mfma_f32_16x16x32_f16 v[174:177], v[242:245], v[210:213], v[174:177]
	v_mfma_f32_16x16x32_f16 v[178:181], v[242:245], v[214:217], v[178:181]
	v_mfma_f32_16x16x32_f16 v[182:185], v[242:245], v[218:221], v[182:185]
	v_mfma_f32_16x16x32_f16 v[154:157], v[242:245], v[222:225], v[154:157]
	s_setprio 0
	ds_read_b128 v[12:15], v130 offset:12288
	ds_read_b128 v[238:241], v130 offset:14336
	v_cvt_pk_f16_f32 v39, v38, v39
	v_cvt_pk_f16_f32 v38, v36, v37
	ds_write_b64 v100, v[38:39] offset:61440
	s_add_u32 s70, s22, 0xe0900
	s_addc_u32 s71, s90, 0
	global_load_dwordx4 v[60:63], v201, s[70:71] nt
	s_setprio 1
	s_waitcnt lgkmcnt(1)
	v_mfma_f32_16x16x32_f16 v[36:39], v[12:15], v[210:213], v[16:19]
	v_mfma_f32_16x16x32_f16 v[32:35], v[12:15], v[214:217], v[32:35]
	v_mfma_f32_16x16x32_f16 v[158:161], v[12:15], v[218:221], v[158:161]
	v_mfma_f32_16x16x32_f16 v[166:169], v[12:15], v[222:225], v[166:169]
	v_mfma_f32_16x16x32_f16 v[190:193], v[238:241], v[210:213], v[190:193]
	v_mfma_f32_16x16x32_f16 v[202:205], v[238:241], v[214:217], v[202:205]
	v_mfma_f32_16x16x32_f16 v[206:209], v[238:241], v[218:221], v[206:209]
	v_mfma_f32_16x16x32_f16 v[186:189], v[238:241], v[222:225], v[186:189]
	s_setprio 0
	s_waitcnt vmcnt(5)
	s_waitcnt lgkmcnt(0)
	s_barrier
	v_add_u32_e32 v250, 0x20000, v129
	v_add_u32_e32 v251, 0x20000, v130
	ds_read_b128 v[210:213], v131 offset:32768
	ds_read_b128 v[214:217], v131 offset:34816
	ds_read_b128 v[218:221], v131 offset:36864
	ds_read_b128 v[222:225], v131 offset:38912
	ds_read_b128 v[12:15], v250
	ds_read_b128 v[16:19], v250 offset:2048
	s_add_u32 s70, s22, 0xa00
	v_lshl_add_u64 v[92:93], s[42:43], 0, v[196:197]
	s_addc_u32 s71, s90, 0
	s_mov_b32 m0, s1
	v_cvt_pk_f16_f32 v3, v2, v3
	global_load_lds_dwordx4 v[92:93], off
	v_cvt_pk_f16_f32 v2, v0, v1
	ds_write_b64 v100, v[2:3]
	global_load_dwordx4 v[0:3], v201, s[70:71] nt
	s_setprio 1
	s_waitcnt lgkmcnt(1)
	v_mfma_f32_16x16x32_f16 v[104:107], v[12:15], v[218:221], v[104:107]
	v_mfma_f32_16x16x32_f16 v[108:111], v[16:19], v[210:213], v[108:111]
	v_mfma_f32_16x16x32_f16 v[112:115], v[16:19], v[214:217], v[112:115]
	v_mfma_f32_16x16x32_f16 v[116:119], v[16:19], v[218:221], v[116:119]
	v_mfma_f32_16x16x32_f16 v[238:241], v[12:15], v[210:213], v[20:23]
	v_mfma_f32_16x16x32_f16 v[230:233], v[12:15], v[214:217], v[230:233]
	v_mfma_f32_16x16x32_f16 v[234:237], v[12:15], v[222:225], v[234:237]
	v_mfma_f32_16x16x32_f16 v[226:229], v[16:19], v[222:225], v[226:229]
	s_setprio 0
	ds_read_b128 v[16:19], v250 offset:4096
	ds_read_b128 v[20:23], v250 offset:6144
	s_mov_b32 m0, s92
	v_lshl_add_u64 v[12:13], v[92:93], 0, s[58:59]
	global_load_lds_dwordx4 v[12:13], off
	v_cvt_pk_f16_f32 v13, v66, v67
	v_cvt_pk_f16_f32 v12, v64, v65
	ds_write_b64 v100, v[12:13] offset:4096
	s_add_u32 s0, s22, 0x20a00
	s_addc_u32 s1, s90, 0
	global_load_dwordx4 v[12:15], v201, s[0:1] nt
	s_setprio 1
	s_waitcnt lgkmcnt(1)
	v_mfma_f32_16x16x32_f16 v[64:67], v[16:19], v[210:213], v[24:27]
	v_mfma_f32_16x16x32_f16 v[120:123], v[16:19], v[222:225], v[120:123]
	v_mfma_f32_16x16x32_f16 v[124:127], v[20:23], v[210:213], v[124:127]
	v_mfma_f32_16x16x32_f16 v[146:149], v[20:23], v[214:217], v[146:149]
	v_mfma_f32_16x16x32_f16 v[134:137], v[20:23], v[222:225], v[134:137]
	v_mfma_f32_16x16x32_f16 v[138:141], v[16:19], v[214:217], v[138:141]
	v_mfma_f32_16x16x32_f16 v[142:145], v[16:19], v[218:221], v[142:145]
	v_mfma_f32_16x16x32_f16 v[150:153], v[20:23], v[218:221], v[150:153]
	s_setprio 0
	ds_read_b128 v[20:23], v250 offset:8192
	ds_read_b128 v[24:27], v250 offset:10240
	s_mov_b32 m0, s91
	v_lshl_add_u64 v[16:17], v[92:93], 0, s[60:61]
	global_load_lds_dwordx4 v[16:17], off
	v_lshl_add_u64 v[252:253], v[92:93], 0, s[62:63]
	s_add_u32 m0, m0, 0x2000
	s_nop 0
	global_load_lds_dwordx4 v[252:253], off
	v_cvt_pk_f16_f32 v17, v70, v71
	v_cvt_pk_f16_f32 v16, v68, v69
	ds_write_b64 v100, v[16:17] offset:8192
	s_add_u32 s0, s22, 0x40a00
	s_addc_u32 s1, s90, 0
	global_load_dwordx4 v[16:19], v201, s[0:1] nt
	s_setprio 1
	s_waitcnt lgkmcnt(1)
	v_mfma_f32_16x16x32_f16 v[68:71], v[20:23], v[210:213], v[246:249]
	v_mfma_f32_16x16x32_f16 v[242:245], v[20:23], v[214:217], v[28:31]
	v_mfma_f32_16x16x32_f16 v[170:173], v[20:23], v[218:221], v[170:173]
	v_mfma_f32_16x16x32_f16 v[162:165], v[20:23], v[222:225], v[162:165]
	v_mfma_f32_16x16x32_f16 v[174:177], v[24:27], v[210:213], v[174:177]
	v_mfma_f32_16x16x32_f16 v[178:181], v[24:27], v[214:217], v[178:181]
	v_mfma_f32_16x16x32_f16 v[182:185], v[24:27], v[218:221], v[182:185]
	v_mfma_f32_16x16x32_f16 v[154:157], v[24:27], v[222:225], v[154:157]
	s_setprio 0
	ds_read_b128 v[24:27], v250 offset:12288
	ds_read_b128 v[28:31], v250 offset:14336
	v_lshl_add_u64 v[20:21], v[92:93], 0, s[62:63]
	v_cvt_pk_f16_f32 v21, v74, v75
	v_cvt_pk_f16_f32 v20, v72, v73
	ds_write_b64 v100, v[20:21] offset:12288
	s_add_u32 s0, s22, 0x60a00
	s_addc_u32 s1, s90, 0
	global_load_dwordx4 v[20:23], v201, s[0:1] nt
	s_setprio 1
	s_waitcnt lgkmcnt(1)
	v_mfma_f32_16x16x32_f16 v[72:75], v[24:27], v[210:213], v[36:39]
	v_mfma_f32_16x16x32_f16 v[246:249], v[24:27], v[214:217], v[32:35]
	v_mfma_f32_16x16x32_f16 v[158:161], v[24:27], v[218:221], v[158:161]
	v_mfma_f32_16x16x32_f16 v[166:169], v[24:27], v[222:225], v[166:169]
	v_mfma_f32_16x16x32_f16 v[190:193], v[28:31], v[210:213], v[190:193]
	v_mfma_f32_16x16x32_f16 v[202:205], v[28:31], v[214:217], v[202:205]
	v_mfma_f32_16x16x32_f16 v[206:209], v[28:31], v[218:221], v[206:209]
	v_mfma_f32_16x16x32_f16 v[186:189], v[28:31], v[222:225], v[186:189]
	s_setprio 0
	ds_read_b128 v[210:213], v128 offset:32768
	ds_read_b128 v[214:217], v128 offset:34816
	ds_read_b128 v[218:221], v128 offset:36864
	ds_read_b128 v[222:225], v128 offset:38912
	ds_read_b128 v[28:31], v251
	ds_read_b128 v[32:35], v251 offset:2048
	v_cvt_pk_f16_f32 v25, v78, v79
	v_cvt_pk_f16_f32 v24, v76, v77
	ds_write_b64 v100, v[24:25] offset:16384
	s_add_u32 s0, s22, 0x80a00
	s_addc_u32 s1, s90, 0
	global_load_dwordx4 v[24:27], v201, s[0:1] nt
	s_setprio 1
	s_waitcnt lgkmcnt(1)
	v_mfma_f32_16x16x32_f16 v[76:79], v[28:31], v[210:213], v[238:241]
	v_mfma_f32_16x16x32_f16 v[104:107], v[28:31], v[218:221], v[104:107]
	v_mfma_f32_16x16x32_f16 v[108:111], v[32:35], v[210:213], v[108:111]
	v_mfma_f32_16x16x32_f16 v[112:115], v[32:35], v[214:217], v[112:115]
	v_mfma_f32_16x16x32_f16 v[116:119], v[32:35], v[218:221], v[116:119]
	v_mfma_f32_16x16x32_f16 v[230:233], v[28:31], v[214:217], v[230:233]
	v_mfma_f32_16x16x32_f16 v[234:237], v[28:31], v[222:225], v[234:237]
	v_mfma_f32_16x16x32_f16 v[226:229], v[32:35], v[222:225], v[226:229]
	s_setprio 0
	ds_read_b128 v[32:35], v251 offset:4096
	ds_read_b128 v[36:39], v251 offset:6144
	v_cvt_pk_f16_f32 v29, v82, v83
	v_cvt_pk_f16_f32 v28, v80, v81
	ds_write_b64 v100, v[28:29] offset:20480
	s_add_u32 s0, s22, 0xa0a00
	s_addc_u32 s1, s90, 0
	global_load_dwordx4 v[28:31], v201, s[0:1] nt
	s_setprio 1
	s_waitcnt lgkmcnt(1)
	v_mfma_f32_16x16x32_f16 v[80:83], v[32:35], v[210:213], v[64:67]
	v_mfma_f32_16x16x32_f16 v[120:123], v[32:35], v[222:225], v[120:123]
	v_mfma_f32_16x16x32_f16 v[124:127], v[36:39], v[210:213], v[124:127]
	v_mfma_f32_16x16x32_f16 v[146:149], v[36:39], v[214:217], v[146:149]
	v_mfma_f32_16x16x32_f16 v[134:137], v[36:39], v[222:225], v[134:137]
	v_mfma_f32_16x16x32_f16 v[138:141], v[32:35], v[214:217], v[138:141]
	v_mfma_f32_16x16x32_f16 v[142:145], v[32:35], v[218:221], v[142:145]
	v_mfma_f32_16x16x32_f16 v[150:153], v[36:39], v[218:221], v[150:153]
	s_setprio 0
	ds_read_b128 v[36:39], v251 offset:8192
	ds_read_b128 v[64:67], v251 offset:10240
	v_cvt_pk_f16_f32 v33, v86, v87
	v_cvt_pk_f16_f32 v32, v84, v85
	ds_write_b64 v100, v[32:33] offset:24576
	s_add_u32 s0, s22, 0xc0a00
	s_addc_u32 s1, s90, 0
	global_load_dwordx4 v[32:35], v201, s[0:1] nt
	s_setprio 1
	s_waitcnt lgkmcnt(1)
	v_mfma_f32_16x16x32_f16 v[68:71], v[36:39], v[210:213], v[68:71]
	v_mfma_f32_16x16x32_f16 v[84:87], v[36:39], v[214:217], v[242:245]
	v_mfma_f32_16x16x32_f16 v[170:173], v[36:39], v[218:221], v[170:173]
	v_mfma_f32_16x16x32_f16 v[162:165], v[36:39], v[222:225], v[162:165]
	v_mfma_f32_16x16x32_f16 v[174:177], v[64:67], v[210:213], v[174:177]
	v_mfma_f32_16x16x32_f16 v[178:181], v[64:67], v[214:217], v[178:181]
	v_mfma_f32_16x16x32_f16 v[182:185], v[64:67], v[218:221], v[182:185]
	v_mfma_f32_16x16x32_f16 v[154:157], v[64:67], v[222:225], v[154:157]
	s_setprio 0
	ds_read_b128 v[64:67], v251 offset:12288
	ds_read_b128 v[238:241], v251 offset:14336
	v_cvt_pk_f16_f32 v37, v90, v91
	v_cvt_pk_f16_f32 v36, v88, v89
	ds_write_b64 v100, v[36:37] offset:28672
	s_add_u32 s0, s22, 0xe0a00
	s_addc_u32 s1, s90, 0
	global_load_dwordx4 v[36:39], v201, s[0:1] nt
	s_setprio 1
	s_waitcnt lgkmcnt(1)
	v_mfma_f32_16x16x32_f16 v[72:75], v[64:67], v[210:213], v[72:75]
	v_mfma_f32_16x16x32_f16 v[88:91], v[64:67], v[214:217], v[246:249]
	v_mfma_f32_16x16x32_f16 v[158:161], v[64:67], v[218:221], v[158:161]
	v_mfma_f32_16x16x32_f16 v[166:169], v[64:67], v[222:225], v[166:169]
	v_mfma_f32_16x16x32_f16 v[190:193], v[238:241], v[210:213], v[190:193]
	v_mfma_f32_16x16x32_f16 v[202:205], v[238:241], v[214:217], v[202:205]
	v_mfma_f32_16x16x32_f16 v[206:209], v[238:241], v[218:221], v[206:209]
	v_mfma_f32_16x16x32_f16 v[186:189], v[238:241], v[222:225], v[186:189]
	s_setprio 0
	s_waitcnt vmcnt(6)
	s_waitcnt lgkmcnt(0)
	s_barrier
	ds_read_b128 v[210:213], v131
	ds_read_b128 v[214:217], v131 offset:2048
	ds_read_b128 v[218:221], v131 offset:4096
	ds_read_b128 v[222:225], v131 offset:6144
	ds_read_b128 v[64:67], v129
	ds_read_b128 v[238:241], v129 offset:2048
	s_add_u32 s70, s22, 0xb00
	v_lshl_add_u64 v[92:93], s[44:45], 0, v[196:197]
	s_addc_u32 s71, s90, 0
	v_readfirstlane_b32 s0, v95
	s_mov_b32 m0, s0
	v_cvt_pk_f16_f32 v7, v6, v7
	global_load_lds_dwordx4 v[92:93], off
	v_cvt_pk_f16_f32 v6, v4, v5
	ds_write_b64 v100, v[6:7] offset:32768
	global_load_dwordx4 v[4:7], v201, s[70:71] nt
	s_setprio 1
	s_waitcnt lgkmcnt(1)
	v_mfma_f32_16x16x32_f16 v[76:79], v[64:67], v[210:213], v[76:79]
	v_mfma_f32_16x16x32_f16 v[104:107], v[64:67], v[218:221], v[104:107]
	v_mfma_f32_16x16x32_f16 v[108:111], v[238:241], v[210:213], v[108:111]
	v_mfma_f32_16x16x32_f16 v[112:115], v[238:241], v[214:217], v[112:115]
	v_mfma_f32_16x16x32_f16 v[116:119], v[238:241], v[218:221], v[116:119]
	v_mfma_f32_16x16x32_f16 v[230:233], v[64:67], v[214:217], v[230:233]
	v_mfma_f32_16x16x32_f16 v[234:237], v[64:67], v[222:225], v[234:237]
	v_mfma_f32_16x16x32_f16 v[226:229], v[238:241], v[222:225], v[226:229]
	s_setprio 0
	ds_read_b128 v[238:241], v129 offset:4096
	ds_read_b128 v[242:245], v129 offset:6144
	v_readfirstlane_b32 s72, v96
	v_lshl_add_u64 v[64:65], v[92:93], 0, s[58:59]
	s_mov_b32 m0, s72
	v_cvt_pk_f16_f32 v11, v10, v11
	global_load_lds_dwordx4 v[64:65], off
	v_cvt_pk_f16_f32 v10, v8, v9
	ds_write_b64 v100, v[10:11] offset:36864
	s_add_u32 s70, s22, 0x20b00
	s_addc_u32 s71, s90, 0
	global_load_dwordx4 v[64:67], v201, s[70:71] nt
	s_setprio 1
	s_waitcnt lgkmcnt(1)
	v_mfma_f32_16x16x32_f16 v[8:11], v[238:241], v[210:213], v[80:83]
	v_mfma_f32_16x16x32_f16 v[80:83], v[238:241], v[214:217], v[138:141]
	v_mfma_f32_16x16x32_f16 v[138:141], v[238:241], v[218:221], v[142:145]
	v_mfma_f32_16x16x32_f16 v[120:123], v[238:241], v[222:225], v[120:123]
	v_mfma_f32_16x16x32_f16 v[124:127], v[242:245], v[210:213], v[124:127]
	v_mfma_f32_16x16x32_f16 v[142:145], v[242:245], v[214:217], v[146:149]
	v_mfma_f32_16x16x32_f16 v[146:149], v[242:245], v[218:221], v[150:153]
	v_mfma_f32_16x16x32_f16 v[134:137], v[242:245], v[222:225], v[134:137]
	s_setprio 0
	s_nop 0
	ds_read_b128 v[150:153], v129 offset:8192
	ds_read_b128 v[238:241], v129 offset:10240
	v_readfirstlane_b32 s71, v97
	v_lshl_add_u64 v[198:199], v[92:93], 0, s[60:61]
	s_mov_b32 m0, s71
	v_cvt_pk_f16_f32 v43, v42, v43
	global_load_lds_dwordx4 v[198:199], off
	v_lshl_add_u64 v[252:253], v[92:93], 0, s[62:63]
	s_add_u32 m0, m0, 0x2000
	s_nop 0
	global_load_lds_dwordx4 v[252:253], off
	v_cvt_pk_f16_f32 v42, v40, v41
	ds_write_b64 v100, v[42:43] offset:40960
	s_add_u32 s80, s22, 0x40b00
	s_addc_u32 s81, s90, 0
	global_load_dwordx4 v[40:43], v201, s[80:81] nt
	s_setprio 1
	s_waitcnt lgkmcnt(1)
	v_mfma_f32_16x16x32_f16 v[68:71], v[150:153], v[210:213], v[68:71]
	v_mfma_f32_16x16x32_f16 v[84:87], v[150:153], v[214:217], v[84:87]
	v_mfma_f32_16x16x32_f16 v[170:173], v[150:153], v[218:221], v[170:173]
	v_mfma_f32_16x16x32_f16 v[150:153], v[150:153], v[222:225], v[162:165]
	v_mfma_f32_16x16x32_f16 v[162:165], v[238:241], v[210:213], v[174:177]
	v_mfma_f32_16x16x32_f16 v[174:177], v[238:241], v[214:217], v[178:181]
	v_mfma_f32_16x16x32_f16 v[178:181], v[238:241], v[218:221], v[182:185]
	v_mfma_f32_16x16x32_f16 v[154:157], v[238:241], v[222:225], v[154:157]
	s_setprio 0
	s_nop 0
	ds_read_b128 v[182:185], v129 offset:12288
	ds_read_b128 v[238:241], v129 offset:14336
	v_readfirstlane_b32 s70, v98
	v_lshl_add_u64 v[92:93], v[92:93], 0, s[62:63]
	v_cvt_pk_f16_f32 v47, v46, v47
	v_cvt_pk_f16_f32 v46, v44, v45
	ds_write_b64 v100, v[46:47] offset:45056
	s_add_u32 s80, s22, 0x60b00
	s_addc_u32 s81, s90, 0
	global_load_dwordx4 v[44:47], v201, s[80:81] nt
	s_setprio 1
	s_waitcnt lgkmcnt(1)
	v_mfma_f32_16x16x32_f16 v[72:75], v[182:185], v[210:213], v[72:75]
	v_mfma_f32_16x16x32_f16 v[88:91], v[182:185], v[214:217], v[88:91]
	v_mfma_f32_16x16x32_f16 v[158:161], v[182:185], v[218:221], v[158:161]
	v_mfma_f32_16x16x32_f16 v[166:169], v[182:185], v[222:225], v[166:169]
	v_mfma_f32_16x16x32_f16 v[182:185], v[238:241], v[210:213], v[190:193]
	v_mfma_f32_16x16x32_f16 v[190:193], v[238:241], v[214:217], v[202:205]
	v_mfma_f32_16x16x32_f16 v[202:205], v[238:241], v[218:221], v[206:209]
	v_mfma_f32_16x16x32_f16 v[186:189], v[238:241], v[222:225], v[186:189]
	s_setprio 0
	s_nop 0
	ds_read_b128 v[206:209], v128
	ds_read_b128 v[210:213], v128 offset:2048
	ds_read_b128 v[214:217], v128 offset:4096
	ds_read_b128 v[218:221], v128 offset:6144
	ds_read_b128 v[222:225], v130
	ds_read_b128 v[238:241], v130 offset:2048
	v_cvt_pk_f16_f32 v51, v50, v51
	v_cvt_pk_f16_f32 v50, v48, v49
	ds_write_b64 v100, v[50:51] offset:49152
	s_add_u32 s80, s22, 0x80b00
	s_addc_u32 s81, s90, 0
	global_load_dwordx4 v[48:51], v201, s[80:81] nt
	s_setprio 1
	s_waitcnt lgkmcnt(1)
	v_mfma_f32_16x16x32_f16 v[76:79], v[222:225], v[206:209], v[76:79]
	v_mfma_f32_16x16x32_f16 v[104:107], v[222:225], v[214:217], v[104:107]
	v_mfma_f32_16x16x32_f16 v[108:111], v[238:241], v[206:209], v[108:111]
	v_mfma_f32_16x16x32_f16 v[112:115], v[238:241], v[210:213], v[112:115]
	v_mfma_f32_16x16x32_f16 v[116:119], v[238:241], v[214:217], v[116:119]
	v_mfma_f32_16x16x32_f16 v[230:233], v[222:225], v[210:213], v[230:233]
	v_mfma_f32_16x16x32_f16 v[222:225], v[222:225], v[218:221], v[234:237]
	v_mfma_f32_16x16x32_f16 v[226:229], v[238:241], v[218:221], v[226:229]
	s_setprio 0
	s_nop 0
	ds_read_b128 v[234:237], v130 offset:4096
	ds_read_b128 v[238:241], v130 offset:6144
	v_cvt_pk_f16_f32 v55, v54, v55
	v_cvt_pk_f16_f32 v54, v52, v53
	ds_write_b64 v100, v[54:55] offset:53248
	s_add_u32 s80, s22, 0xa0b00
	s_addc_u32 s81, s90, 0
	global_load_dwordx4 v[52:55], v201, s[80:81] nt
	s_setprio 1
	s_waitcnt lgkmcnt(1)
	v_mfma_f32_16x16x32_f16 v[80:83], v[234:237], v[210:213], v[80:83]
	v_mfma_f32_16x16x32_f16 v[120:123], v[234:237], v[218:221], v[120:123]
	v_mfma_f32_16x16x32_f16 v[124:127], v[238:241], v[206:209], v[124:127]
	v_mfma_f32_16x16x32_f16 v[146:149], v[238:241], v[214:217], v[146:149]
	v_mfma_f32_16x16x32_f16 v[134:137], v[238:241], v[218:221], v[134:137]
	v_mfma_f32_16x16x32_f16 v[242:245], v[234:237], v[206:209], v[8:11]
	v_mfma_f32_16x16x32_f16 v[138:141], v[234:237], v[214:217], v[138:141]
	v_mfma_f32_16x16x32_f16 v[142:145], v[238:241], v[210:213], v[142:145]
	s_setprio 0
	ds_read_b128 v[8:11], v130 offset:8192
	ds_read_b128 v[234:237], v130 offset:10240
	v_cvt_pk_f16_f32 v59, v58, v59
	v_cvt_pk_f16_f32 v58, v56, v57
	ds_write_b64 v100, v[58:59] offset:57344
	s_add_u32 s80, s22, 0xc0b00
	s_addc_u32 s81, s90, 0
	global_load_dwordx4 v[56:59], v201, s[80:81] nt
	s_setprio 1
	s_waitcnt lgkmcnt(1)
	v_mfma_f32_16x16x32_f16 v[84:87], v[8:11], v[210:213], v[84:87]
	v_mfma_f32_16x16x32_f16 v[238:241], v[8:11], v[206:209], v[68:71]
	v_mfma_f32_16x16x32_f16 v[170:173], v[8:11], v[214:217], v[170:173]
	v_mfma_f32_16x16x32_f16 v[150:153], v[8:11], v[218:221], v[150:153]
	v_mfma_f32_16x16x32_f16 v[162:165], v[234:237], v[206:209], v[162:165]
	v_mfma_f32_16x16x32_f16 v[174:177], v[234:237], v[210:213], v[174:177]
	v_mfma_f32_16x16x32_f16 v[178:181], v[234:237], v[214:217], v[178:181]
	v_mfma_f32_16x16x32_f16 v[154:157], v[234:237], v[218:221], v[154:157]
	s_setprio 0
	ds_read_b128 v[8:11], v130 offset:12288
	ds_read_b128 v[68:71], v130 offset:14336
	v_cvt_pk_f16_f32 v63, v62, v63
	v_cvt_pk_f16_f32 v62, v60, v61
	ds_write_b64 v100, v[62:63] offset:61440
	s_add_u32 s80, s22, 0xe0b00
	s_addc_u32 s81, s90, 0
	global_load_dwordx4 v[60:63], v201, s[80:81] nt
	s_setprio 1
	s_waitcnt lgkmcnt(1)
	v_mfma_f32_16x16x32_f16 v[88:91], v[8:11], v[210:213], v[88:91]
	v_mfma_f32_16x16x32_f16 v[234:237], v[8:11], v[206:209], v[72:75]
	v_mfma_f32_16x16x32_f16 v[158:161], v[8:11], v[214:217], v[158:161]
	v_mfma_f32_16x16x32_f16 v[166:169], v[8:11], v[218:221], v[166:169]
	v_mfma_f32_16x16x32_f16 v[182:185], v[68:71], v[206:209], v[182:185]
	v_mfma_f32_16x16x32_f16 v[190:193], v[68:71], v[210:213], v[190:193]
	v_mfma_f32_16x16x32_f16 v[202:205], v[68:71], v[214:217], v[202:205]
	v_mfma_f32_16x16x32_f16 v[186:189], v[68:71], v[218:221], v[186:189]
	s_setprio 0
	s_waitcnt vmcnt(6)
	s_waitcnt lgkmcnt(0)
	s_barrier
	ds_read_b128 v[206:209], v131 offset:32768
	ds_read_b128 v[210:213], v131 offset:34816
	ds_read_b128 v[214:217], v131 offset:36864
	ds_read_b128 v[218:221], v131 offset:38912
	ds_read_b128 v[68:71], v129 offset:32768
	ds_read_b128 v[72:75], v129 offset:34816
	s_add_u32 s80, s22, 0xc00
	v_lshl_add_u64 v[92:93], s[46:47], 0, v[196:197]
	s_addc_u32 s81, s90, 0
	v_readfirstlane_b32 s1, v94
	s_mov_b32 m0, s1
	v_cvt_pk_f16_f32 v3, v2, v3
	global_load_lds_dwordx4 v[92:93], off
	v_cvt_pk_f16_f32 v2, v0, v1
	ds_write_b64 v100, v[2:3]
	global_load_dwordx4 v[8:11], v201, s[80:81] nt
	s_setprio 1
	s_waitcnt lgkmcnt(1)
	v_mfma_f32_16x16x32_f16 v[0:3], v[68:71], v[206:209], v[76:79]
	v_mfma_f32_16x16x32_f16 v[104:107], v[68:71], v[214:217], v[104:107]
	v_mfma_f32_16x16x32_f16 v[108:111], v[72:75], v[206:209], v[108:111]
	v_mfma_f32_16x16x32_f16 v[112:115], v[72:75], v[210:213], v[112:115]
	v_mfma_f32_16x16x32_f16 v[116:119], v[72:75], v[214:217], v[116:119]
	v_mfma_f32_16x16x32_f16 v[230:233], v[68:71], v[210:213], v[230:233]
	v_mfma_f32_16x16x32_f16 v[222:225], v[68:71], v[218:221], v[222:225]
	v_mfma_f32_16x16x32_f16 v[226:229], v[72:75], v[218:221], v[226:229]
	s_setprio 0
	ds_read_b128 v[72:75], v129 offset:36864
	ds_read_b128 v[76:79], v129 offset:38912
	v_readfirstlane_b32 s92, v99
	v_lshl_add_u64 v[68:69], v[92:93], 0, s[58:59]
	s_mov_b32 m0, s92
	v_cvt_pk_f16_f32 v15, v14, v15
	global_load_lds_dwordx4 v[68:69], off
	v_cvt_pk_f16_f32 v14, v12, v13
	ds_write_b64 v100, v[14:15] offset:4096
	s_add_u32 s80, s22, 0x20c00
	s_addc_u32 s81, s90, 0
	global_load_dwordx4 v[68:71], v201, s[80:81] nt
	s_setprio 1
	s_waitcnt lgkmcnt(1)
	v_mfma_f32_16x16x32_f16 v[12:15], v[72:75], v[206:209], v[242:245]
	v_mfma_f32_16x16x32_f16 v[120:123], v[72:75], v[218:221], v[120:123]
	v_mfma_f32_16x16x32_f16 v[124:127], v[76:79], v[206:209], v[124:127]
	v_mfma_f32_16x16x32_f16 v[146:149], v[76:79], v[214:217], v[146:149]
	v_mfma_f32_16x16x32_f16 v[134:137], v[76:79], v[218:221], v[134:137]
	v_mfma_f32_16x16x32_f16 v[242:245], v[72:75], v[210:213], v[80:83]
	v_mfma_f32_16x16x32_f16 v[138:141], v[72:75], v[214:217], v[138:141]
	v_mfma_f32_16x16x32_f16 v[142:145], v[76:79], v[210:213], v[142:145]
	s_setprio 0
	ds_read_b128 v[76:79], v129 offset:40960
	ds_read_b128 v[80:83], v129 offset:43008
	v_readfirstlane_b32 s91, v101
	v_lshl_add_u64 v[72:73], v[92:93], 0, s[60:61]
	s_mov_b32 m0, s91
	v_cvt_pk_f16_f32 v19, v18, v19
	global_load_lds_dwordx4 v[72:73], off
	v_lshl_add_u64 v[252:253], v[92:93], 0, s[62:63]
	s_add_u32 m0, m0, 0x2000
	s_nop 0
	global_load_lds_dwordx4 v[252:253], off
	v_cvt_pk_f16_f32 v18, v16, v17
	ds_write_b64 v100, v[18:19] offset:8192
	s_add_u32 s80, s22, 0x40c00
	s_addc_u32 s81, s90, 0
	global_load_dwordx4 v[72:75], v201, s[80:81] nt
	s_setprio 1
	s_waitcnt lgkmcnt(1)
	v_mfma_f32_16x16x32_f16 v[16:19], v[76:79], v[206:209], v[238:241]
	v_mfma_f32_16x16x32_f16 v[238:241], v[76:79], v[210:213], v[84:87]
	v_mfma_f32_16x16x32_f16 v[170:173], v[76:79], v[214:217], v[170:173]
	v_mfma_f32_16x16x32_f16 v[150:153], v[76:79], v[218:221], v[150:153]
	v_mfma_f32_16x16x32_f16 v[162:165], v[80:83], v[206:209], v[162:165]
	v_mfma_f32_16x16x32_f16 v[174:177], v[80:83], v[210:213], v[174:177]
	v_mfma_f32_16x16x32_f16 v[178:181], v[80:83], v[214:217], v[178:181]
	v_mfma_f32_16x16x32_f16 v[154:157], v[80:83], v[218:221], v[154:157]
	s_setprio 0
	ds_read_b128 v[80:83], v129 offset:45056
	ds_read_b128 v[84:87], v129 offset:47104
	v_readfirstlane_b32 s73, v102
	v_lshl_add_u64 v[76:77], v[92:93], 0, s[62:63]
	v_cvt_pk_f16_f32 v23, v22, v23
	v_cvt_pk_f16_f32 v22, v20, v21
	ds_write_b64 v100, v[22:23] offset:12288
	s_add_u32 s80, s22, 0x60c00
	s_addc_u32 s81, s90, 0
	global_load_dwordx4 v[76:79], v201, s[80:81] nt
	s_setprio 1
	s_waitcnt lgkmcnt(1)
	v_mfma_f32_16x16x32_f16 v[20:23], v[80:83], v[206:209], v[234:237]
	v_mfma_f32_16x16x32_f16 v[234:237], v[80:83], v[210:213], v[88:91]
	v_mfma_f32_16x16x32_f16 v[158:161], v[80:83], v[214:217], v[158:161]
	v_mfma_f32_16x16x32_f16 v[166:169], v[80:83], v[218:221], v[166:169]
	v_mfma_f32_16x16x32_f16 v[182:185], v[84:87], v[206:209], v[182:185]
	v_mfma_f32_16x16x32_f16 v[190:193], v[84:87], v[210:213], v[190:193]
	v_mfma_f32_16x16x32_f16 v[202:205], v[84:87], v[214:217], v[202:205]
	v_mfma_f32_16x16x32_f16 v[186:189], v[84:87], v[218:221], v[186:189]
	s_setprio 0
	ds_read_b128 v[206:209], v128 offset:32768
	ds_read_b128 v[210:213], v128 offset:34816
	ds_read_b128 v[214:217], v128 offset:36864
	ds_read_b128 v[218:221], v128 offset:38912
	ds_read_b128 v[84:87], v130 offset:32768
	ds_read_b128 v[88:91], v130 offset:34816
	v_cvt_pk_f16_f32 v27, v26, v27
	v_cvt_pk_f16_f32 v26, v24, v25
	ds_write_b64 v100, v[26:27] offset:16384
	s_add_u32 s80, s22, 0x80c00
	s_addc_u32 s81, s90, 0
	global_load_dwordx4 v[80:83], v201, s[80:81] nt
	s_setprio 1
	s_waitcnt lgkmcnt(1)
	v_mfma_f32_16x16x32_f16 v[24:27], v[84:87], v[206:209], v[0:3]
	v_mfma_f32_16x16x32_f16 v[104:107], v[84:87], v[214:217], v[104:107]
	v_mfma_f32_16x16x32_f16 v[108:111], v[88:91], v[206:209], v[108:111]
	v_mfma_f32_16x16x32_f16 v[112:115], v[88:91], v[210:213], v[112:115]
	v_mfma_f32_16x16x32_f16 v[116:119], v[88:91], v[214:217], v[116:119]
	v_mfma_f32_16x16x32_f16 v[230:233], v[84:87], v[210:213], v[230:233]
	v_mfma_f32_16x16x32_f16 v[222:225], v[84:87], v[218:221], v[222:225]
	v_mfma_f32_16x16x32_f16 v[226:229], v[88:91], v[218:221], v[226:229]
	s_setprio 0
	ds_read_b128 v[0:3], v130 offset:36864
	ds_read_b128 v[88:91], v130 offset:38912
	v_cvt_pk_f16_f32 v31, v30, v31
	v_cvt_pk_f16_f32 v30, v28, v29
	ds_write_b64 v100, v[30:31] offset:20480
	s_add_u32 s80, s22, 0xa0c00
	s_addc_u32 s81, s90, 0
	global_load_dwordx4 v[84:87], v201, s[80:81] nt
	s_setprio 1
	s_waitcnt lgkmcnt(1)
	v_mfma_f32_16x16x32_f16 v[12:15], v[0:3], v[206:209], v[12:15]
	v_mfma_f32_16x16x32_f16 v[28:31], v[0:3], v[210:213], v[242:245]
	v_mfma_f32_16x16x32_f16 v[120:123], v[0:3], v[218:221], v[120:123]
	v_mfma_f32_16x16x32_f16 v[124:127], v[88:91], v[206:209], v[124:127]
	v_mfma_f32_16x16x32_f16 v[146:149], v[88:91], v[214:217], v[146:149]
	v_mfma_f32_16x16x32_f16 v[134:137], v[88:91], v[218:221], v[134:137]
	v_mfma_f32_16x16x32_f16 v[138:141], v[0:3], v[214:217], v[138:141]
	v_mfma_f32_16x16x32_f16 v[142:145], v[88:91], v[210:213], v[142:145]
	s_setprio 0
	ds_read_b128 v[0:3], v130 offset:40960
	ds_read_b128 v[242:245], v130 offset:43008
	v_cvt_pk_f16_f32 v35, v34, v35
	v_cvt_pk_f16_f32 v34, v32, v33
	ds_write_b64 v100, v[34:35] offset:24576
	s_add_u32 s80, s22, 0xc0c00
	s_addc_u32 s81, s90, 0
	global_load_dwordx4 v[88:91], v201, s[80:81] nt
	s_setprio 1
	s_waitcnt lgkmcnt(1)
	v_mfma_f32_16x16x32_f16 v[16:19], v[0:3], v[206:209], v[16:19]
	v_mfma_f32_16x16x32_f16 v[32:35], v[0:3], v[210:213], v[238:241]
	v_mfma_f32_16x16x32_f16 v[170:173], v[0:3], v[214:217], v[170:173]
	v_mfma_f32_16x16x32_f16 v[150:153], v[0:3], v[218:221], v[150:153]
	v_mfma_f32_16x16x32_f16 v[162:165], v[242:245], v[206:209], v[162:165]
	v_mfma_f32_16x16x32_f16 v[174:177], v[242:245], v[210:213], v[174:177]
	v_mfma_f32_16x16x32_f16 v[178:181], v[242:245], v[214:217], v[178:181]
	v_mfma_f32_16x16x32_f16 v[154:157], v[242:245], v[218:221], v[154:157]
	s_setprio 0
	ds_read_b128 v[0:3], v130 offset:45056
	ds_read_b128 v[238:241], v130 offset:47104
	v_cvt_pk_f16_f32 v39, v38, v39
	v_cvt_pk_f16_f32 v38, v36, v37
	ds_write_b64 v100, v[38:39] offset:28672
	s_add_u32 s80, s22, 0xe0c00
	s_addc_u32 s81, s90, 0
	global_load_dwordx4 v[36:39], v201, s[80:81] nt
	s_setprio 1
	s_waitcnt lgkmcnt(1)
	v_mfma_f32_16x16x32_f16 v[20:23], v[0:3], v[206:209], v[20:23]
	v_mfma_f32_16x16x32_f16 v[234:237], v[0:3], v[210:213], v[234:237]
	v_mfma_f32_16x16x32_f16 v[158:161], v[0:3], v[214:217], v[158:161]
	v_mfma_f32_16x16x32_f16 v[166:169], v[0:3], v[218:221], v[166:169]
	v_mfma_f32_16x16x32_f16 v[182:185], v[238:241], v[206:209], v[182:185]
	v_mfma_f32_16x16x32_f16 v[190:193], v[238:241], v[210:213], v[190:193]
	v_mfma_f32_16x16x32_f16 v[202:205], v[238:241], v[214:217], v[202:205]
	v_mfma_f32_16x16x32_f16 v[186:189], v[238:241], v[218:221], v[186:189]
	s_setprio 0
	s_waitcnt vmcnt(6)
	s_waitcnt lgkmcnt(0)
	s_barrier
	ds_read_b128 v[206:209], v131
	ds_read_b128 v[210:213], v131 offset:2048
	ds_read_b128 v[214:217], v131 offset:4096
	ds_read_b128 v[218:221], v131 offset:6144
	ds_read_b128 v[238:241], v129
	ds_read_b128 v[242:245], v129 offset:2048
	s_add_u32 s80, s22, 0xd00
	v_lshl_add_u64 v[92:93], s[48:49], 0, v[196:197]
	s_addc_u32 s81, s90, 0
	s_mov_b32 m0, s0
	v_cvt_pk_f16_f32 v1, v6, v7
	global_load_lds_dwordx4 v[92:93], off
	v_cvt_pk_f16_f32 v0, v4, v5
	ds_write_b64 v100, v[0:1] offset:32768
	global_load_dwordx4 v[0:3], v201, s[80:81] nt
	s_setprio 1
	s_waitcnt lgkmcnt(1)
	v_mfma_f32_16x16x32_f16 v[24:27], v[238:241], v[206:209], v[24:27]
	v_mfma_f32_16x16x32_f16 v[104:107], v[238:241], v[214:217], v[104:107]
	v_mfma_f32_16x16x32_f16 v[108:111], v[242:245], v[206:209], v[108:111]
	v_mfma_f32_16x16x32_f16 v[112:115], v[242:245], v[210:213], v[112:115]
	v_mfma_f32_16x16x32_f16 v[116:119], v[242:245], v[214:217], v[116:119]
	v_mfma_f32_16x16x32_f16 v[230:233], v[238:241], v[210:213], v[230:233]
	v_mfma_f32_16x16x32_f16 v[222:225], v[238:241], v[218:221], v[222:225]
	v_mfma_f32_16x16x32_f16 v[226:229], v[242:245], v[218:221], v[226:229]
	s_setprio 0
	ds_read_b128 v[238:241], v129 offset:4096
	ds_read_b128 v[242:245], v129 offset:6144
	s_mov_b32 m0, s72
	v_lshl_add_u64 v[4:5], v[92:93], 0, s[58:59]
	global_load_lds_dwordx4 v[4:5], off
	v_cvt_pk_f16_f32 v5, v66, v67
	v_cvt_pk_f16_f32 v4, v64, v65
	ds_write_b64 v100, v[4:5] offset:36864
	s_add_u32 s80, s22, 0x20d00
	s_addc_u32 s81, s90, 0
	global_load_dwordx4 v[4:7], v201, s[80:81] nt
	s_setprio 1
	s_waitcnt lgkmcnt(1)
	v_mfma_f32_16x16x32_f16 v[64:67], v[238:241], v[206:209], v[12:15]
	v_mfma_f32_16x16x32_f16 v[28:31], v[238:241], v[210:213], v[28:31]
	v_mfma_f32_16x16x32_f16 v[120:123], v[238:241], v[218:221], v[120:123]
	v_mfma_f32_16x16x32_f16 v[124:127], v[242:245], v[206:209], v[124:127]
	v_mfma_f32_16x16x32_f16 v[146:149], v[242:245], v[214:217], v[146:149]
	v_mfma_f32_16x16x32_f16 v[134:137], v[242:245], v[218:221], v[134:137]
	v_mfma_f32_16x16x32_f16 v[138:141], v[238:241], v[214:217], v[138:141]
	v_mfma_f32_16x16x32_f16 v[142:145], v[242:245], v[210:213], v[142:145]
	s_setprio 0
	ds_read_b128 v[238:241], v129 offset:8192
	ds_read_b128 v[242:245], v129 offset:10240
	s_mov_b32 m0, s71
	v_lshl_add_u64 v[12:13], v[92:93], 0, s[60:61]
	global_load_lds_dwordx4 v[12:13], off
	v_lshl_add_u64 v[252:253], v[92:93], 0, s[62:63]
	s_add_u32 m0, m0, 0x2000
	s_nop 0
	global_load_lds_dwordx4 v[252:253], off
	v_cvt_pk_f16_f32 v13, v42, v43
	v_cvt_pk_f16_f32 v12, v40, v41
	ds_write_b64 v100, v[12:13] offset:40960
	s_add_u32 s80, s22, 0x40d00
	s_addc_u32 s81, s90, 0
	global_load_dwordx4 v[12:15], v201, s[80:81] nt
	s_setprio 1
	s_waitcnt lgkmcnt(1)
	v_mfma_f32_16x16x32_f16 v[40:43], v[238:241], v[206:209], v[16:19]
	v_mfma_f32_16x16x32_f16 v[32:35], v[238:241], v[210:213], v[32:35]
	v_mfma_f32_16x16x32_f16 v[170:173], v[238:241], v[214:217], v[170:173]
	v_mfma_f32_16x16x32_f16 v[150:153], v[238:241], v[218:221], v[150:153]
	v_mfma_f32_16x16x32_f16 v[162:165], v[242:245], v[206:209], v[162:165]
	v_mfma_f32_16x16x32_f16 v[174:177], v[242:245], v[210:213], v[174:177]
	v_mfma_f32_16x16x32_f16 v[178:181], v[242:245], v[214:217], v[178:181]
	v_mfma_f32_16x16x32_f16 v[154:157], v[242:245], v[218:221], v[154:157]
	s_setprio 0
	ds_read_b128 v[238:241], v129 offset:12288
	ds_read_b128 v[242:245], v129 offset:14336
	v_lshl_add_u64 v[16:17], v[92:93], 0, s[62:63]
	v_cvt_pk_f16_f32 v17, v46, v47
	v_cvt_pk_f16_f32 v16, v44, v45
	ds_write_b64 v100, v[16:17] offset:45056
	s_add_u32 s70, s22, 0x60d00
	s_addc_u32 s71, s90, 0
	global_load_dwordx4 v[16:19], v201, s[70:71] nt
	s_setprio 1
	s_waitcnt lgkmcnt(1)
	v_mfma_f32_16x16x32_f16 v[44:47], v[238:241], v[206:209], v[20:23]
	v_mfma_f32_16x16x32_f16 v[234:237], v[238:241], v[210:213], v[234:237]
	v_mfma_f32_16x16x32_f16 v[158:161], v[238:241], v[214:217], v[158:161]
	v_mfma_f32_16x16x32_f16 v[166:169], v[238:241], v[218:221], v[166:169]
	v_mfma_f32_16x16x32_f16 v[182:185], v[242:245], v[206:209], v[182:185]
	v_mfma_f32_16x16x32_f16 v[190:193], v[242:245], v[210:213], v[190:193]
	v_mfma_f32_16x16x32_f16 v[202:205], v[242:245], v[214:217], v[202:205]
	v_mfma_f32_16x16x32_f16 v[186:189], v[242:245], v[218:221], v[186:189]
	s_setprio 0
	ds_read_b128 v[206:209], v128
	ds_read_b128 v[210:213], v128 offset:2048
	ds_read_b128 v[214:217], v128 offset:4096
	ds_read_b128 v[218:221], v128 offset:6144
	ds_read_b128 v[238:241], v130
	ds_read_b128 v[242:245], v130 offset:2048
	v_cvt_pk_f16_f32 v21, v50, v51
	v_cvt_pk_f16_f32 v20, v48, v49
	ds_write_b64 v100, v[20:21] offset:49152
	s_add_u32 s70, s22, 0x80d00
	s_addc_u32 s71, s90, 0
	global_load_dwordx4 v[20:23], v201, s[70:71] nt
	s_setprio 1
	s_waitcnt lgkmcnt(1)
	v_mfma_f32_16x16x32_f16 v[48:51], v[238:241], v[206:209], v[24:27]
	v_mfma_f32_16x16x32_f16 v[104:107], v[238:241], v[214:217], v[104:107]
	v_mfma_f32_16x16x32_f16 v[108:111], v[242:245], v[206:209], v[108:111]
	v_mfma_f32_16x16x32_f16 v[112:115], v[242:245], v[210:213], v[112:115]
	v_mfma_f32_16x16x32_f16 v[116:119], v[242:245], v[214:217], v[116:119]
	v_mfma_f32_16x16x32_f16 v[230:233], v[238:241], v[210:213], v[230:233]
	v_mfma_f32_16x16x32_f16 v[222:225], v[238:241], v[218:221], v[222:225]
	v_mfma_f32_16x16x32_f16 v[226:229], v[242:245], v[218:221], v[226:229]
	s_setprio 0
	ds_read_b128 v[238:241], v130 offset:4096
	ds_read_b128 v[242:245], v130 offset:6144
	v_cvt_pk_f16_f32 v25, v54, v55
	v_cvt_pk_f16_f32 v24, v52, v53
	ds_write_b64 v100, v[24:25] offset:53248
	s_add_u32 s70, s22, 0xa0d00
	s_addc_u32 s71, s90, 0
	global_load_dwordx4 v[24:27], v201, s[70:71] nt
	s_setprio 1
	s_waitcnt lgkmcnt(1)
	v_mfma_f32_16x16x32_f16 v[52:55], v[238:241], v[206:209], v[64:67]
	v_mfma_f32_16x16x32_f16 v[64:67], v[238:241], v[210:213], v[28:31]
	v_mfma_f32_16x16x32_f16 v[120:123], v[238:241], v[218:221], v[120:123]
	v_mfma_f32_16x16x32_f16 v[124:127], v[242:245], v[206:209], v[124:127]
	v_mfma_f32_16x16x32_f16 v[146:149], v[242:245], v[214:217], v[146:149]
	v_mfma_f32_16x16x32_f16 v[134:137], v[242:245], v[218:221], v[134:137]
	v_mfma_f32_16x16x32_f16 v[138:141], v[238:241], v[214:217], v[138:141]
	v_mfma_f32_16x16x32_f16 v[142:145], v[242:245], v[210:213], v[142:145]
	s_setprio 0
	ds_read_b128 v[238:241], v130 offset:8192
	ds_read_b128 v[242:245], v130 offset:10240
	v_cvt_pk_f16_f32 v29, v58, v59
	v_cvt_pk_f16_f32 v28, v56, v57
	ds_write_b64 v100, v[28:29] offset:57344
	s_add_u32 s70, s22, 0xc0d00
	s_addc_u32 s71, s90, 0
	global_load_dwordx4 v[28:31], v201, s[70:71] nt
	s_setprio 1
	s_waitcnt lgkmcnt(1)
	v_mfma_f32_16x16x32_f16 v[56:59], v[238:241], v[206:209], v[40:43]
	v_mfma_f32_16x16x32_f16 v[246:249], v[238:241], v[210:213], v[32:35]
	v_mfma_f32_16x16x32_f16 v[170:173], v[238:241], v[214:217], v[170:173]
	v_mfma_f32_16x16x32_f16 v[150:153], v[238:241], v[218:221], v[150:153]
	v_mfma_f32_16x16x32_f16 v[162:165], v[242:245], v[206:209], v[162:165]
	v_mfma_f32_16x16x32_f16 v[174:177], v[242:245], v[210:213], v[174:177]
	v_mfma_f32_16x16x32_f16 v[178:181], v[242:245], v[214:217], v[178:181]
	v_mfma_f32_16x16x32_f16 v[154:157], v[242:245], v[218:221], v[154:157]
	s_setprio 0
	ds_read_b128 v[40:43], v130 offset:12288
	ds_read_b128 v[238:241], v130 offset:14336
	v_cvt_pk_f16_f32 v33, v62, v63
	v_cvt_pk_f16_f32 v32, v60, v61
	ds_write_b64 v100, v[32:33] offset:61440
	s_add_u32 s70, s22, 0xe0d00
	s_addc_u32 s71, s90, 0
	global_load_dwordx4 v[32:35], v201, s[70:71] nt
	s_setprio 1
	s_waitcnt lgkmcnt(1)
	v_mfma_f32_16x16x32_f16 v[60:63], v[40:43], v[206:209], v[44:47]
	v_mfma_f32_16x16x32_f16 v[234:237], v[40:43], v[210:213], v[234:237]
	v_mfma_f32_16x16x32_f16 v[158:161], v[40:43], v[214:217], v[158:161]
	v_mfma_f32_16x16x32_f16 v[166:169], v[40:43], v[218:221], v[166:169]
	v_mfma_f32_16x16x32_f16 v[182:185], v[238:241], v[206:209], v[182:185]
	v_mfma_f32_16x16x32_f16 v[190:193], v[238:241], v[210:213], v[190:193]
	v_mfma_f32_16x16x32_f16 v[202:205], v[238:241], v[214:217], v[202:205]
	v_mfma_f32_16x16x32_f16 v[186:189], v[238:241], v[218:221], v[186:189]
	s_setprio 0
	s_waitcnt vmcnt(6)
	s_waitcnt lgkmcnt(0)
	s_barrier
	ds_read_b128 v[206:209], v131 offset:32768
	ds_read_b128 v[210:213], v131 offset:34816
	ds_read_b128 v[214:217], v131 offset:36864
	ds_read_b128 v[218:221], v131 offset:38912
	ds_read_b128 v[40:43], v129 offset:32768
	ds_read_b128 v[44:47], v129 offset:34816
	s_add_u32 s70, s22, 0xe00
	v_lshl_add_u64 v[92:93], s[50:51], 0, v[196:197]
	s_addc_u32 s71, s90, 0
	s_mov_b32 m0, s1
	v_cvt_pk_f16_f32 v11, v10, v11
	global_load_lds_dwordx4 v[92:93], off
	v_cvt_pk_f16_f32 v10, v8, v9
	ds_write_b64 v100, v[10:11]
	global_load_dwordx4 v[8:11], v201, s[70:71] nt
	s_setprio 1
	s_waitcnt lgkmcnt(1)
	v_mfma_f32_16x16x32_f16 v[104:107], v[40:43], v[214:217], v[104:107]
	v_mfma_f32_16x16x32_f16 v[108:111], v[44:47], v[206:209], v[108:111]
	v_mfma_f32_16x16x32_f16 v[112:115], v[44:47], v[210:213], v[112:115]
	v_mfma_f32_16x16x32_f16 v[116:119], v[44:47], v[214:217], v[116:119]
	v_mfma_f32_16x16x32_f16 v[238:241], v[40:43], v[206:209], v[48:51]
	v_mfma_f32_16x16x32_f16 v[230:233], v[40:43], v[210:213], v[230:233]
	v_mfma_f32_16x16x32_f16 v[222:225], v[40:43], v[218:221], v[222:225]
	v_mfma_f32_16x16x32_f16 v[226:229], v[44:47], v[218:221], v[226:229]
	s_setprio 0
	ds_read_b128 v[44:47], v129 offset:36864
	ds_read_b128 v[48:51], v129 offset:38912
	s_mov_b32 m0, s92
	v_lshl_add_u64 v[40:41], v[92:93], 0, s[58:59]
	global_load_lds_dwordx4 v[40:41], off
	v_cvt_pk_f16_f32 v41, v70, v71
	v_cvt_pk_f16_f32 v40, v68, v69
	ds_write_b64 v100, v[40:41] offset:4096
	s_add_u32 s0, s22, 0x20e00
	s_addc_u32 s1, s90, 0
	global_load_dwordx4 v[40:43], v201, s[0:1] nt
	s_setprio 1
	s_waitcnt lgkmcnt(1)
	v_mfma_f32_16x16x32_f16 v[68:71], v[44:47], v[206:209], v[52:55]
	v_mfma_f32_16x16x32_f16 v[64:67], v[44:47], v[210:213], v[64:67]
	v_mfma_f32_16x16x32_f16 v[120:123], v[44:47], v[218:221], v[120:123]
	v_mfma_f32_16x16x32_f16 v[124:127], v[48:51], v[206:209], v[124:127]
	v_mfma_f32_16x16x32_f16 v[146:149], v[48:51], v[214:217], v[146:149]
	v_mfma_f32_16x16x32_f16 v[134:137], v[48:51], v[218:221], v[134:137]
	v_mfma_f32_16x16x32_f16 v[138:141], v[44:47], v[214:217], v[138:141]
	v_mfma_f32_16x16x32_f16 v[142:145], v[48:51], v[210:213], v[142:145]
	s_setprio 0
	ds_read_b128 v[48:51], v129 offset:40960
	ds_read_b128 v[52:55], v129 offset:43008
	s_mov_b32 m0, s91
	v_lshl_add_u64 v[44:45], v[92:93], 0, s[60:61]
	global_load_lds_dwordx4 v[44:45], off
	v_lshl_add_u64 v[252:253], v[92:93], 0, s[62:63]
	s_add_u32 m0, m0, 0x2000
	s_nop 0
	global_load_lds_dwordx4 v[252:253], off
	v_cvt_pk_f16_f32 v45, v74, v75
	v_cvt_pk_f16_f32 v44, v72, v73
	ds_write_b64 v100, v[44:45] offset:8192
	s_add_u32 s0, s22, 0x40e00
	s_addc_u32 s1, s90, 0
	global_load_dwordx4 v[44:47], v201, s[0:1] nt
	s_setprio 1
	s_waitcnt lgkmcnt(1)
	v_mfma_f32_16x16x32_f16 v[72:75], v[48:51], v[206:209], v[56:59]
	v_mfma_f32_16x16x32_f16 v[242:245], v[48:51], v[210:213], v[246:249]
	v_mfma_f32_16x16x32_f16 v[170:173], v[48:51], v[214:217], v[170:173]
	v_mfma_f32_16x16x32_f16 v[150:153], v[48:51], v[218:221], v[150:153]
	v_mfma_f32_16x16x32_f16 v[162:165], v[52:55], v[206:209], v[162:165]
	v_mfma_f32_16x16x32_f16 v[174:177], v[52:55], v[210:213], v[174:177]
	v_mfma_f32_16x16x32_f16 v[178:181], v[52:55], v[214:217], v[178:181]
	v_mfma_f32_16x16x32_f16 v[154:157], v[52:55], v[218:221], v[154:157]
	s_setprio 0
	ds_read_b128 v[52:55], v129 offset:45056
	ds_read_b128 v[56:59], v129 offset:47104
	v_lshl_add_u64 v[48:49], v[92:93], 0, s[62:63]
	v_cvt_pk_f16_f32 v49, v78, v79
	v_cvt_pk_f16_f32 v48, v76, v77
	ds_write_b64 v100, v[48:49] offset:12288
	s_add_u32 s0, s22, 0x60e00
	s_addc_u32 s1, s90, 0
	global_load_dwordx4 v[48:51], v201, s[0:1] nt
	s_setprio 1
	s_waitcnt lgkmcnt(1)
	v_mfma_f32_16x16x32_f16 v[76:79], v[52:55], v[206:209], v[60:63]
	v_mfma_f32_16x16x32_f16 v[234:237], v[52:55], v[210:213], v[234:237]
	v_mfma_f32_16x16x32_f16 v[158:161], v[52:55], v[214:217], v[158:161]
	v_mfma_f32_16x16x32_f16 v[166:169], v[52:55], v[218:221], v[166:169]
	v_mfma_f32_16x16x32_f16 v[182:185], v[56:59], v[206:209], v[182:185]
	v_mfma_f32_16x16x32_f16 v[190:193], v[56:59], v[210:213], v[190:193]
	v_mfma_f32_16x16x32_f16 v[202:205], v[56:59], v[214:217], v[202:205]
	v_mfma_f32_16x16x32_f16 v[186:189], v[56:59], v[218:221], v[186:189]
	s_setprio 0
	ds_read_b128 v[206:209], v128 offset:32768
	ds_read_b128 v[210:213], v128 offset:34816
	ds_read_b128 v[214:217], v128 offset:36864
	ds_read_b128 v[218:221], v128 offset:38912
	ds_read_b128 v[56:59], v130 offset:32768
	ds_read_b128 v[60:63], v130 offset:34816
	v_cvt_pk_f16_f32 v53, v82, v83
	v_cvt_pk_f16_f32 v52, v80, v81
	ds_write_b64 v100, v[52:53] offset:16384
	s_add_u32 s0, s22, 0x80e00
	s_addc_u32 s1, s90, 0
	global_load_dwordx4 v[52:55], v201, s[0:1] nt
	s_setprio 1
	s_waitcnt lgkmcnt(1)
	v_mfma_f32_16x16x32_f16 v[80:83], v[56:59], v[206:209], v[238:241]
	v_mfma_f32_16x16x32_f16 v[104:107], v[56:59], v[214:217], v[104:107]
	v_mfma_f32_16x16x32_f16 v[108:111], v[60:63], v[206:209], v[108:111]
	v_mfma_f32_16x16x32_f16 v[112:115], v[60:63], v[210:213], v[112:115]
	v_mfma_f32_16x16x32_f16 v[116:119], v[60:63], v[214:217], v[116:119]
	v_mfma_f32_16x16x32_f16 v[230:233], v[56:59], v[210:213], v[230:233]
	v_mfma_f32_16x16x32_f16 v[222:225], v[56:59], v[218:221], v[222:225]
	v_mfma_f32_16x16x32_f16 v[226:229], v[60:63], v[218:221], v[226:229]
	s_setprio 0
	ds_read_b128 v[60:63], v130 offset:36864
	ds_read_b128 v[238:241], v130 offset:38912
	v_cvt_pk_f16_f32 v57, v86, v87
	v_cvt_pk_f16_f32 v56, v84, v85
	ds_write_b64 v100, v[56:57] offset:20480
	s_add_u32 s0, s22, 0xa0e00
	s_addc_u32 s1, s90, 0
	global_load_dwordx4 v[56:59], v201, s[0:1] nt
	s_setprio 1
	s_waitcnt lgkmcnt(1)
	v_mfma_f32_16x16x32_f16 v[68:71], v[60:63], v[206:209], v[68:71]
	v_mfma_f32_16x16x32_f16 v[64:67], v[60:63], v[210:213], v[64:67]
	v_mfma_f32_16x16x32_f16 v[84:87], v[60:63], v[214:217], v[138:141]
	v_mfma_f32_16x16x32_f16 v[120:123], v[60:63], v[218:221], v[120:123]
	v_mfma_f32_16x16x32_f16 v[124:127], v[238:241], v[206:209], v[124:127]
	v_mfma_f32_16x16x32_f16 v[134:137], v[238:241], v[218:221], v[134:137]
	v_mfma_f32_16x16x32_f16 v[138:141], v[238:241], v[210:213], v[142:145]
	v_mfma_f32_16x16x32_f16 v[142:145], v[238:241], v[214:217], v[146:149]
	s_setprio 0
	s_nop 1
	ds_read_b128 v[146:149], v130 offset:40960
	ds_read_b128 v[238:241], v130 offset:43008
	v_cvt_pk_f16_f32 v61, v90, v91
	v_cvt_pk_f16_f32 v60, v88, v89
	ds_write_b64 v100, v[60:61] offset:24576
	s_add_u32 s0, s22, 0xc0e00
	s_addc_u32 s1, s90, 0
	global_load_dwordx4 v[60:63], v201, s[0:1] nt
	s_setprio 1
	s_waitcnt lgkmcnt(1)
	v_mfma_f32_16x16x32_f16 v[72:75], v[146:149], v[206:209], v[72:75]
	v_mfma_f32_16x16x32_f16 v[88:91], v[146:149], v[210:213], v[242:245]
	v_mfma_f32_16x16x32_f16 v[170:173], v[146:149], v[214:217], v[170:173]
	v_mfma_f32_16x16x32_f16 v[146:149], v[146:149], v[218:221], v[150:153]
	v_mfma_f32_16x16x32_f16 v[150:153], v[238:241], v[206:209], v[162:165]
	v_mfma_f32_16x16x32_f16 v[162:165], v[238:241], v[210:213], v[174:177]
	v_mfma_f32_16x16x32_f16 v[174:177], v[238:241], v[214:217], v[178:181]
	v_mfma_f32_16x16x32_f16 v[154:157], v[238:241], v[218:221], v[154:157]
	s_setprio 0
	s_nop 0
	ds_read_b128 v[178:181], v130 offset:45056
	ds_read_b128 v[238:241], v130 offset:47104
	v_cvt_pk_f16_f32 v39, v38, v39
	v_cvt_pk_f16_f32 v38, v36, v37
	ds_write_b64 v100, v[38:39] offset:28672
	s_add_u32 s0, s22, 0xe0e00
	s_addc_u32 s1, s90, 0
	global_load_dwordx4 v[36:39], v201, s[0:1] nt
	s_setprio 1
	s_waitcnt lgkmcnt(1)
	v_mfma_f32_16x16x32_f16 v[76:79], v[178:181], v[206:209], v[76:79]
	v_mfma_f32_16x16x32_f16 v[234:237], v[178:181], v[210:213], v[234:237]
	v_mfma_f32_16x16x32_f16 v[158:161], v[178:181], v[214:217], v[158:161]
	v_mfma_f32_16x16x32_f16 v[166:169], v[178:181], v[218:221], v[166:169]
	v_mfma_f32_16x16x32_f16 v[178:181], v[238:241], v[206:209], v[182:185]
	v_mfma_f32_16x16x32_f16 v[182:185], v[238:241], v[210:213], v[190:193]
	v_mfma_f32_16x16x32_f16 v[190:193], v[238:241], v[214:217], v[202:205]
	v_mfma_f32_16x16x32_f16 v[186:189], v[238:241], v[218:221], v[186:189]
	s_setprio 0
	s_waitcnt vmcnt(6)
	s_waitcnt lgkmcnt(0)
	s_barrier
	ds_read_b128 v[202:205], v131
	ds_read_b128 v[206:209], v131 offset:2048
	ds_read_b128 v[210:213], v131 offset:4096
	ds_read_b128 v[214:217], v131 offset:6144
	ds_read_b128 v[218:221], v129
	ds_read_b128 v[238:241], v129 offset:2048
	s_add_u32 s70, s22, 0xf00
	v_lshl_add_u64 v[92:93], s[52:53], 0, v[196:197]
	s_addc_u32 s71, s90, 0
	v_readfirstlane_b32 s0, v95
	s_mov_b32 m0, s0
	v_cvt_pk_f16_f32 v3, v2, v3
	global_load_lds_dwordx4 v[92:93], off
	v_cvt_pk_f16_f32 v2, v0, v1
	ds_write_b64 v100, v[2:3] offset:32768
	global_load_dwordx4 v[0:3], v201, s[70:71] nt
	s_setprio 1
	s_waitcnt lgkmcnt(1)
	v_mfma_f32_16x16x32_f16 v[80:83], v[218:221], v[202:205], v[80:83]
	v_mfma_f32_16x16x32_f16 v[104:107], v[218:221], v[210:213], v[104:107]
	v_mfma_f32_16x16x32_f16 v[108:111], v[238:241], v[202:205], v[108:111]
	v_mfma_f32_16x16x32_f16 v[112:115], v[238:241], v[206:209], v[112:115]
	v_mfma_f32_16x16x32_f16 v[116:119], v[238:241], v[210:213], v[116:119]
	v_mfma_f32_16x16x32_f16 v[230:233], v[218:221], v[206:209], v[230:233]
	v_mfma_f32_16x16x32_f16 v[218:221], v[218:221], v[214:217], v[222:225]
	v_mfma_f32_16x16x32_f16 v[222:225], v[238:241], v[214:217], v[226:229]
	s_setprio 0
	s_nop 1
	ds_read_b128 v[226:229], v129 offset:4096
	ds_read_b128 v[238:241], v129 offset:6144
	v_readfirstlane_b32 s1, v96
	v_lshl_add_u64 v[198:199], v[92:93], 0, s[58:59]
	s_mov_b32 m0, s1
	v_cvt_pk_f16_f32 v7, v6, v7
	global_load_lds_dwordx4 v[198:199], off
	v_cvt_pk_f16_f32 v6, v4, v5
	ds_write_b64 v100, v[6:7] offset:36864
	s_add_u32 s70, s22, 0x20f00
	s_addc_u32 s71, s90, 0
	global_load_dwordx4 v[4:7], v201, s[70:71] nt
	s_setprio 1
	s_waitcnt lgkmcnt(1)
	v_mfma_f32_16x16x32_f16 v[68:71], v[226:229], v[202:205], v[68:71]
	v_mfma_f32_16x16x32_f16 v[64:67], v[226:229], v[206:209], v[64:67]
	v_mfma_f32_16x16x32_f16 v[84:87], v[226:229], v[210:213], v[84:87]
	v_mfma_f32_16x16x32_f16 v[120:123], v[226:229], v[214:217], v[120:123]
	v_mfma_f32_16x16x32_f16 v[124:127], v[238:241], v[202:205], v[124:127]
	v_mfma_f32_16x16x32_f16 v[134:137], v[238:241], v[214:217], v[134:137]
	v_mfma_f32_16x16x32_f16 v[138:141], v[238:241], v[206:209], v[138:141]
	v_mfma_f32_16x16x32_f16 v[142:145], v[238:241], v[210:213], v[142:145]
	s_setprio 0
	ds_read_b128 v[226:229], v129 offset:8192
	ds_read_b128 v[238:241], v129 offset:10240
	v_readfirstlane_b32 s70, v97
	v_lshl_add_u64 v[198:199], v[92:93], 0, s[60:61]
	s_mov_b32 m0, s70
	v_cvt_pk_f16_f32 v15, v14, v15
	global_load_lds_dwordx4 v[198:199], off
	v_lshl_add_u64 v[252:253], v[92:93], 0, s[62:63]
	s_add_u32 m0, m0, 0x2000
	s_nop 0
	global_load_lds_dwordx4 v[252:253], off
	v_cvt_pk_f16_f32 v14, v12, v13
	ds_write_b64 v100, v[14:15] offset:40960
	s_add_u32 s72, s22, 0x40f00
	s_addc_u32 s73, s90, 0
	global_load_dwordx4 v[12:15], v201, s[72:73] nt
	s_setprio 1
	s_waitcnt lgkmcnt(1)
	v_mfma_f32_16x16x32_f16 v[72:75], v[226:229], v[202:205], v[72:75]
	v_mfma_f32_16x16x32_f16 v[88:91], v[226:229], v[206:209], v[88:91]
	v_mfma_f32_16x16x32_f16 v[146:149], v[226:229], v[214:217], v[146:149]
	v_mfma_f32_16x16x32_f16 v[170:173], v[226:229], v[210:213], v[170:173]
	v_mfma_f32_16x16x32_f16 v[150:153], v[238:241], v[202:205], v[150:153]
	v_mfma_f32_16x16x32_f16 v[162:165], v[238:241], v[206:209], v[162:165]
	v_mfma_f32_16x16x32_f16 v[174:177], v[238:241], v[210:213], v[174:177]
	v_mfma_f32_16x16x32_f16 v[154:157], v[238:241], v[214:217], v[154:157]
	s_setprio 0
	ds_read_b128 v[226:229], v129 offset:12288
	ds_read_b128 v[238:241], v129 offset:14336
	v_readfirstlane_b32 s71, v98
	v_lshl_add_u64 v[92:93], v[92:93], 0, s[62:63]
	v_cvt_pk_f16_f32 v19, v18, v19
	v_cvt_pk_f16_f32 v18, v16, v17
	ds_write_b64 v100, v[18:19] offset:45056
	s_add_u32 s72, s22, 0x60f00
	s_addc_u32 s73, s90, 0
	global_load_dwordx4 v[16:19], v201, s[72:73] nt
	s_setprio 1
	s_waitcnt lgkmcnt(1)
	v_mfma_f32_16x16x32_f16 v[76:79], v[226:229], v[202:205], v[76:79]
	v_mfma_f32_16x16x32_f16 v[234:237], v[226:229], v[206:209], v[234:237]
	v_mfma_f32_16x16x32_f16 v[158:161], v[226:229], v[210:213], v[158:161]
	v_mfma_f32_16x16x32_f16 v[166:169], v[226:229], v[214:217], v[166:169]
	v_mfma_f32_16x16x32_f16 v[178:181], v[238:241], v[202:205], v[178:181]
	v_mfma_f32_16x16x32_f16 v[182:185], v[238:241], v[206:209], v[182:185]
	v_mfma_f32_16x16x32_f16 v[190:193], v[238:241], v[210:213], v[190:193]
	v_mfma_f32_16x16x32_f16 v[186:189], v[238:241], v[214:217], v[186:189]
	s_setprio 0
	ds_read_b128 v[202:205], v128
	ds_read_b128 v[206:209], v128 offset:2048
	ds_read_b128 v[210:213], v128 offset:4096
	ds_read_b128 v[214:217], v128 offset:6144
	ds_read_b128 v[226:229], v130
	ds_read_b128 v[238:241], v130 offset:2048
	v_cvt_pk_f16_f32 v23, v22, v23
	v_cvt_pk_f16_f32 v22, v20, v21
	ds_write_b64 v100, v[22:23] offset:49152
	s_add_u32 s72, s22, 0x80f00
	s_addc_u32 s73, s90, 0
	global_load_dwordx4 v[20:23], v201, s[72:73] nt
	s_setprio 1
	s_waitcnt lgkmcnt(1)
	v_mfma_f32_16x16x32_f16 v[80:83], v[226:229], v[202:205], v[80:83]
	v_mfma_f32_16x16x32_f16 v[104:107], v[226:229], v[210:213], v[104:107]
	v_mfma_f32_16x16x32_f16 v[108:111], v[238:241], v[202:205], v[108:111]
	v_mfma_f32_16x16x32_f16 v[112:115], v[238:241], v[206:209], v[112:115]
	v_mfma_f32_16x16x32_f16 v[116:119], v[238:241], v[210:213], v[116:119]
	v_mfma_f32_16x16x32_f16 v[230:233], v[226:229], v[206:209], v[230:233]
	v_mfma_f32_16x16x32_f16 v[218:221], v[226:229], v[214:217], v[218:221]
	v_mfma_f32_16x16x32_f16 v[222:225], v[238:241], v[214:217], v[222:225]
	s_setprio 0
	ds_read_b128 v[226:229], v130 offset:4096
	ds_read_b128 v[238:241], v130 offset:6144
	v_cvt_pk_f16_f32 v27, v26, v27
	v_cvt_pk_f16_f32 v26, v24, v25
	ds_write_b64 v100, v[26:27] offset:53248
	s_add_u32 s72, s22, 0xa0f00
	s_addc_u32 s73, s90, 0
	global_load_dwordx4 v[24:27], v201, s[72:73] nt
	s_setprio 1
	s_waitcnt lgkmcnt(1)
	v_mfma_f32_16x16x32_f16 v[68:71], v[226:229], v[202:205], v[68:71]
	v_mfma_f32_16x16x32_f16 v[64:67], v[226:229], v[206:209], v[64:67]
	v_mfma_f32_16x16x32_f16 v[84:87], v[226:229], v[210:213], v[84:87]
	v_mfma_f32_16x16x32_f16 v[120:123], v[226:229], v[214:217], v[120:123]
	v_mfma_f32_16x16x32_f16 v[124:127], v[238:241], v[202:205], v[124:127]
	v_mfma_f32_16x16x32_f16 v[134:137], v[238:241], v[214:217], v[134:137]
	v_mfma_f32_16x16x32_f16 v[138:141], v[238:241], v[206:209], v[138:141]
	v_mfma_f32_16x16x32_f16 v[142:145], v[238:241], v[210:213], v[142:145]
	s_setprio 0
	ds_read_b128 v[226:229], v130 offset:8192
	ds_read_b128 v[238:241], v130 offset:10240
	v_cvt_pk_f16_f32 v31, v30, v31
	v_cvt_pk_f16_f32 v30, v28, v29
	ds_write_b64 v100, v[30:31] offset:57344
	s_add_u32 s72, s22, 0xc0f00
	s_addc_u32 s73, s90, 0
	global_load_dwordx4 v[28:31], v201, s[72:73] nt
	s_setprio 1
	s_waitcnt lgkmcnt(1)
	v_mfma_f32_16x16x32_f16 v[72:75], v[226:229], v[202:205], v[72:75]
	v_mfma_f32_16x16x32_f16 v[88:91], v[226:229], v[206:209], v[88:91]
	v_mfma_f32_16x16x32_f16 v[146:149], v[226:229], v[214:217], v[146:149]
	v_mfma_f32_16x16x32_f16 v[170:173], v[226:229], v[210:213], v[170:173]
	v_mfma_f32_16x16x32_f16 v[150:153], v[238:241], v[202:205], v[150:153]
	v_mfma_f32_16x16x32_f16 v[162:165], v[238:241], v[206:209], v[162:165]
	v_mfma_f32_16x16x32_f16 v[174:177], v[238:241], v[210:213], v[174:177]
	v_mfma_f32_16x16x32_f16 v[154:157], v[238:241], v[214:217], v[154:157]
	s_setprio 0
	ds_read_b128 v[226:229], v130 offset:12288
	ds_read_b128 v[238:241], v130 offset:14336
	v_cvt_pk_f16_f32 v35, v34, v35
	v_cvt_pk_f16_f32 v34, v32, v33
	ds_write_b64 v100, v[34:35] offset:61440
	s_add_u32 s72, s22, 0xe0f00
	s_addc_u32 s73, s90, 0
	global_load_dwordx4 v[32:35], v201, s[72:73] nt
	s_setprio 1
	s_waitcnt lgkmcnt(1)
	v_mfma_f32_16x16x32_f16 v[76:79], v[226:229], v[202:205], v[76:79]
	v_mfma_f32_16x16x32_f16 v[234:237], v[226:229], v[206:209], v[234:237]
	v_mfma_f32_16x16x32_f16 v[158:161], v[226:229], v[210:213], v[158:161]
	v_mfma_f32_16x16x32_f16 v[166:169], v[226:229], v[214:217], v[166:169]
	v_mfma_f32_16x16x32_f16 v[178:181], v[238:241], v[202:205], v[178:181]
	v_mfma_f32_16x16x32_f16 v[182:185], v[238:241], v[206:209], v[182:185]
	v_mfma_f32_16x16x32_f16 v[190:193], v[238:241], v[210:213], v[190:193]
	v_mfma_f32_16x16x32_f16 v[186:189], v[238:241], v[214:217], v[186:189]
	s_setprio 0
	s_waitcnt vmcnt(6)
	s_waitcnt lgkmcnt(0)
	s_barrier
	ds_read_b128 v[202:205], v131 offset:32768
	ds_read_b128 v[206:209], v131 offset:34816
	ds_read_b128 v[210:213], v131 offset:36864
	ds_read_b128 v[214:217], v131 offset:38912
	ds_read_b128 v[226:229], v129 offset:32768
	ds_read_b128 v[238:241], v129 offset:34816
	v_lshl_add_u64 v[198:199], s[54:55], 0, v[196:197]
	v_readfirstlane_b32 s64, v94
	s_mov_b32 m0, s64
	v_cvt_pk_f16_f32 v11, v10, v11
	global_load_lds_dwordx4 v[198:199], off
	v_cvt_pk_f16_f32 v10, v8, v9
	ds_write_b64 v100, v[10:11]
	s_setprio 1
	s_waitcnt lgkmcnt(1)
	v_mfma_f32_16x16x32_f16 v[8:11], v[226:229], v[202:205], v[80:83]
	v_mfma_f32_16x16x32_f16 v[80:83], v[226:229], v[206:209], v[230:233]
	v_mfma_f32_16x16x32_f16 v[92:95], v[226:229], v[210:213], v[104:107]
	v_mfma_f32_16x16x32_f16 v[104:107], v[226:229], v[214:217], v[218:221]
	v_mfma_f32_16x16x32_f16 v[108:111], v[238:241], v[202:205], v[108:111]
	v_mfma_f32_16x16x32_f16 v[112:115], v[238:241], v[206:209], v[112:115]
	v_mfma_f32_16x16x32_f16 v[116:119], v[238:241], v[210:213], v[116:119]
	v_mfma_f32_16x16x32_f16 v[218:221], v[238:241], v[214:217], v[222:225]
	s_setprio 0
	s_nop 1
	ds_read_b128 v[222:225], v129 offset:36864
	ds_read_b128 v[226:229], v129 offset:38912
	v_readfirstlane_b32 s64, v99
	v_lshl_add_u64 v[96:97], v[198:199], 0, s[58:59]
	s_mov_b32 m0, s64
	v_cvt_pk_f16_f32 v43, v42, v43
	global_load_lds_dwordx4 v[96:97], off
	v_cvt_pk_f16_f32 v42, v40, v41
	ds_write_b64 v100, v[42:43] offset:4096
	s_setprio 1
	s_waitcnt lgkmcnt(1)
	v_mfma_f32_16x16x32_f16 v[40:43], v[222:225], v[202:205], v[68:71]
	v_mfma_f32_16x16x32_f16 v[64:67], v[222:225], v[206:209], v[64:67]
	v_mfma_f32_16x16x32_f16 v[68:71], v[222:225], v[210:213], v[84:87]
	v_mfma_f32_16x16x32_f16 v[84:87], v[222:225], v[214:217], v[120:123]
	v_mfma_f32_16x16x32_f16 v[96:99], v[226:229], v[202:205], v[124:127]
	v_mfma_f32_16x16x32_f16 v[120:123], v[226:229], v[206:209], v[138:141]
	v_mfma_f32_16x16x32_f16 v[124:127], v[226:229], v[210:213], v[142:145]
	v_mfma_f32_16x16x32_f16 v[134:137], v[226:229], v[214:217], v[134:137]
	s_setprio 0
	ds_read_b128 v[138:141], v129 offset:40960
	ds_read_b128 v[142:145], v129 offset:43008
	v_readfirstlane_b32 s64, v101
	v_lshl_add_u64 v[222:223], v[198:199], 0, s[60:61]
	s_mov_b32 m0, s64
	v_cvt_pk_f16_f32 v47, v46, v47
	global_load_lds_dwordx4 v[222:223], off
	v_cvt_pk_f16_f32 v46, v44, v45
	ds_write_b64 v100, v[46:47] offset:8192
	s_setprio 1
	s_waitcnt lgkmcnt(1)
	v_mfma_f32_16x16x32_f16 v[44:47], v[138:141], v[202:205], v[72:75]
	v_mfma_f32_16x16x32_f16 v[72:75], v[138:141], v[206:209], v[88:91]
	v_mfma_f32_16x16x32_f16 v[88:91], v[138:141], v[210:213], v[170:173]
	v_mfma_f32_16x16x32_f16 v[138:141], v[138:141], v[214:217], v[146:149]
	v_mfma_f32_16x16x32_f16 v[146:149], v[142:145], v[202:205], v[150:153]
	v_mfma_f32_16x16x32_f16 v[150:153], v[142:145], v[206:209], v[162:165]
	v_mfma_f32_16x16x32_f16 v[162:165], v[142:145], v[210:213], v[174:177]
	v_mfma_f32_16x16x32_f16 v[142:145], v[142:145], v[214:217], v[154:157]
	s_setprio 0
	s_nop 1
	ds_read_b128 v[154:157], v129 offset:45056
	ds_read_b128 v[170:173], v129 offset:47104
	v_readfirstlane_b32 s64, v102
	v_lshl_add_u64 v[174:175], v[198:199], 0, s[62:63]
	s_mov_b32 m0, s64
	v_cvt_pk_f16_f32 v51, v50, v51
	global_load_lds_dwordx4 v[174:175], off
	v_cvt_pk_f16_f32 v50, v48, v49
	ds_write_b64 v100, v[50:51] offset:12288
	s_setprio 1
	s_waitcnt lgkmcnt(1)
	v_mfma_f32_16x16x32_f16 v[48:51], v[154:157], v[202:205], v[76:79]
	v_mfma_f32_16x16x32_f16 v[76:79], v[154:157], v[206:209], v[234:237]
	v_mfma_f32_16x16x32_f16 v[158:161], v[154:157], v[210:213], v[158:161]
	v_mfma_f32_16x16x32_f16 v[154:157], v[154:157], v[214:217], v[166:169]
	v_mfma_f32_16x16x32_f16 v[166:169], v[170:173], v[202:205], v[178:181]
	v_mfma_f32_16x16x32_f16 v[174:177], v[170:173], v[206:209], v[182:185]
	v_mfma_f32_16x16x32_f16 v[178:181], v[170:173], v[210:213], v[190:193]
	v_mfma_f32_16x16x32_f16 v[170:173], v[170:173], v[214:217], v[186:189]
	s_setprio 0
	ds_read_b128 v[182:185], v128 offset:32768
	s_nop 0
	ds_read_b128 v[186:189], v128 offset:34816
	ds_read_b128 v[190:193], v128 offset:36864
	ds_read_b128 v[202:205], v128 offset:38912
	ds_read_b128 v[206:209], v130 offset:32768
	ds_read_b128 v[210:213], v130 offset:34816
	v_cvt_pk_f16_f32 v55, v54, v55
	v_cvt_pk_f16_f32 v54, v52, v53
	ds_write_b64 v100, v[54:55] offset:16384
	s_setprio 1
	s_waitcnt lgkmcnt(1)
	v_mfma_f32_16x16x32_f16 v[8:11], v[206:209], v[182:185], v[8:11]
	v_mfma_f32_16x16x32_f16 v[52:55], v[206:209], v[186:189], v[80:83]
	v_mfma_f32_16x16x32_f16 v[80:83], v[206:209], v[190:193], v[92:95]
	v_mfma_f32_16x16x32_f16 v[92:95], v[206:209], v[202:205], v[104:107]
	v_mfma_f32_16x16x32_f16 v[102:105], v[210:213], v[182:185], v[108:111]
	v_mfma_f32_16x16x32_f16 v[106:109], v[210:213], v[186:189], v[112:115]
	v_mfma_f32_16x16x32_f16 v[110:113], v[210:213], v[190:193], v[116:119]
	v_mfma_f32_16x16x32_f16 v[114:117], v[210:213], v[202:205], v[218:221]
	s_setprio 0
	ds_read_b128 v[206:209], v130 offset:36864
	ds_read_b128 v[210:213], v130 offset:38912
	v_cvt_pk_f16_f32 v59, v58, v59
	v_cvt_pk_f16_f32 v58, v56, v57
	ds_write_b64 v100, v[58:59] offset:20480
	s_setprio 1
	s_waitcnt lgkmcnt(1)
	v_mfma_f32_16x16x32_f16 v[40:43], v[206:209], v[182:185], v[40:43]
	v_mfma_f32_16x16x32_f16 v[56:59], v[206:209], v[186:189], v[64:67]
	v_mfma_f32_16x16x32_f16 v[64:67], v[206:209], v[190:193], v[68:71]
	v_mfma_f32_16x16x32_f16 v[68:71], v[206:209], v[202:205], v[84:87]
	v_mfma_f32_16x16x32_f16 v[84:87], v[210:213], v[182:185], v[96:99]
	v_mfma_f32_16x16x32_f16 v[96:99], v[210:213], v[186:189], v[120:123]
	v_mfma_f32_16x16x32_f16 v[118:121], v[210:213], v[190:193], v[124:127]
	v_mfma_f32_16x16x32_f16 v[122:125], v[210:213], v[202:205], v[134:137]
	s_setprio 0
	s_nop 1
	ds_read_b128 v[134:137], v130 offset:40960
	ds_read_b128 v[206:209], v130 offset:43008
	v_cvt_pk_f16_f32 v63, v62, v63
	v_cvt_pk_f16_f32 v62, v60, v61
	ds_write_b64 v100, v[62:63] offset:24576
	s_setprio 1
	s_waitcnt lgkmcnt(1)
	v_mfma_f32_16x16x32_f16 v[44:47], v[134:137], v[182:185], v[44:47]
	v_mfma_f32_16x16x32_f16 v[60:63], v[134:137], v[186:189], v[72:75]
	v_mfma_f32_16x16x32_f16 v[72:75], v[134:137], v[190:193], v[88:91]
	v_mfma_f32_16x16x32_f16 v[88:91], v[134:137], v[202:205], v[138:141]
	v_mfma_f32_16x16x32_f16 v[134:137], v[206:209], v[182:185], v[146:149]
	v_mfma_f32_16x16x32_f16 v[146:149], v[206:209], v[190:193], v[162:165]
	v_mfma_f32_16x16x32_f16 v[138:141], v[206:209], v[186:189], v[150:153]
	v_mfma_f32_16x16x32_f16 v[142:145], v[206:209], v[202:205], v[142:145]
	s_setprio 0
	s_nop 0
	ds_read_b128 v[150:153], v130 offset:45056
	ds_read_b128 v[162:165], v130 offset:47104
	v_cvt_pk_f16_f32 v39, v38, v39
	v_cvt_pk_f16_f32 v38, v36, v37
	ds_write_b64 v100, v[38:39] offset:28672
	s_setprio 1
	s_waitcnt lgkmcnt(1)
	v_mfma_f32_16x16x32_f16 v[36:39], v[150:153], v[182:185], v[48:51]
	v_mfma_f32_16x16x32_f16 v[48:51], v[150:153], v[186:189], v[76:79]
	v_mfma_f32_16x16x32_f16 v[76:79], v[150:153], v[190:193], v[158:161]
	v_mfma_f32_16x16x32_f16 v[150:153], v[150:153], v[202:205], v[154:157]
	v_mfma_f32_16x16x32_f16 v[154:157], v[162:165], v[182:185], v[166:169]
	v_mfma_f32_16x16x32_f16 v[158:161], v[162:165], v[186:189], v[174:177]
	v_mfma_f32_16x16x32_f16 v[166:169], v[162:165], v[190:193], v[178:181]
	v_mfma_f32_16x16x32_f16 v[162:165], v[162:165], v[202:205], v[170:173]
	s_setprio 0
	s_waitcnt vmcnt(0)
	s_waitcnt lgkmcnt(0)
	s_barrier
	s_nop 0
	ds_read_b128 v[170:173], v131
	ds_read_b128 v[174:177], v131 offset:2048
	ds_read_b128 v[178:181], v131 offset:4096
	ds_read_b128 v[182:185], v131 offset:6144
	ds_read_b128 v[186:189], v129
	ds_read_b128 v[190:193], v129 offset:2048
	v_lshl_add_u64 v[126:127], s[56:57], 0, v[196:197]
	s_mov_b32 m0, s0
	v_cvt_pk_f16_f32 v3, v2, v3
	global_load_lds_dwordx4 v[126:127], off
	v_cvt_pk_f16_f32 v2, v0, v1
	ds_write_b64 v100, v[2:3] offset:32768
	s_setprio 1
	s_waitcnt lgkmcnt(1)
	v_mfma_f32_16x16x32_f16 v[0:3], v[186:189], v[170:173], v[8:11]
	v_mfma_f32_16x16x32_f16 v[8:11], v[186:189], v[174:177], v[52:55]
	v_mfma_f32_16x16x32_f16 v[52:55], v[186:189], v[178:181], v[80:83]
	v_mfma_f32_16x16x32_f16 v[80:83], v[186:189], v[182:185], v[92:95]
	v_mfma_f32_16x16x32_f16 v[92:95], v[190:193], v[170:173], v[102:105]
	v_mfma_f32_16x16x32_f16 v[102:105], v[190:193], v[174:177], v[106:109]
	v_mfma_f32_16x16x32_f16 v[106:109], v[190:193], v[178:181], v[110:113]
	v_mfma_f32_16x16x32_f16 v[110:113], v[190:193], v[182:185], v[114:117]
	s_setprio 0
	s_nop 1
	ds_read_b128 v[114:117], v129 offset:4096
	ds_read_b128 v[186:189], v129 offset:6144
	s_mov_b32 m0, s1
	v_lshl_add_u64 v[190:191], v[126:127], 0, s[58:59]
	global_load_lds_dwordx4 v[190:191], off
	v_cvt_pk_f16_f32 v7, v6, v7
	v_cvt_pk_f16_f32 v6, v4, v5
	ds_write_b64 v100, v[6:7] offset:36864
	s_setprio 1
	s_waitcnt lgkmcnt(1)
	v_mfma_f32_16x16x32_f16 v[190:193], v[114:117], v[170:173], v[40:43]
	v_mfma_f32_16x16x32_f16 v[56:59], v[114:117], v[174:177], v[56:59]
	v_mfma_f32_16x16x32_f16 v[64:67], v[114:117], v[178:181], v[64:67]
	v_mfma_f32_16x16x32_f16 v[68:71], v[114:117], v[182:185], v[68:71]
	v_mfma_f32_16x16x32_f16 v[84:87], v[186:189], v[170:173], v[84:87]
	v_mfma_f32_16x16x32_f16 v[96:99], v[186:189], v[174:177], v[96:99]
	v_mfma_f32_16x16x32_f16 v[114:117], v[186:189], v[178:181], v[118:121]
	v_mfma_f32_16x16x32_f16 v[118:121], v[186:189], v[182:185], v[122:125]
	s_setprio 0
	ds_read_b128 v[4:7], v129 offset:8192
	ds_read_b128 v[40:43], v129 offset:10240
	s_mov_b32 m0, s70
	v_lshl_add_u64 v[122:123], v[126:127], 0, s[60:61]
	global_load_lds_dwordx4 v[122:123], off
	v_cvt_pk_f16_f32 v15, v14, v15
	v_cvt_pk_f16_f32 v14, v12, v13
	ds_write_b64 v100, v[14:15] offset:40960
	s_setprio 1
	s_waitcnt lgkmcnt(1)
	v_mfma_f32_16x16x32_f16 v[122:125], v[4:7], v[170:173], v[44:47]
	v_mfma_f32_16x16x32_f16 v[88:91], v[4:7], v[182:185], v[88:91]
	v_mfma_f32_16x16x32_f16 v[134:137], v[40:43], v[170:173], v[134:137]
	v_mfma_f32_16x16x32_f16 v[146:149], v[40:43], v[178:181], v[146:149]
	v_mfma_f32_16x16x32_f16 v[186:189], v[4:7], v[174:177], v[60:63]
	v_mfma_f32_16x16x32_f16 v[202:205], v[4:7], v[178:181], v[72:75]
	v_mfma_f32_16x16x32_f16 v[138:141], v[40:43], v[174:177], v[138:141]
	v_mfma_f32_16x16x32_f16 v[142:145], v[40:43], v[182:185], v[142:145]
	s_setprio 0
	ds_read_b128 v[4:7], v129 offset:12288
	ds_read_b128 v[12:15], v129 offset:14336
	s_mov_b32 m0, s71
	v_lshl_add_u64 v[40:41], v[126:127], 0, s[62:63]
	global_load_lds_dwordx4 v[40:41], off
	v_cvt_pk_f16_f32 v19, v18, v19
	v_cvt_pk_f16_f32 v18, v16, v17
	ds_write_b64 v100, v[18:19] offset:45056
	s_setprio 1
	s_waitcnt lgkmcnt(1)
	v_mfma_f32_16x16x32_f16 v[206:209], v[4:7], v[170:173], v[36:39]
	v_mfma_f32_16x16x32_f16 v[210:213], v[4:7], v[174:177], v[48:51]
	v_mfma_f32_16x16x32_f16 v[214:217], v[4:7], v[178:181], v[76:79]
	v_mfma_f32_16x16x32_f16 v[150:153], v[4:7], v[182:185], v[150:153]
	v_mfma_f32_16x16x32_f16 v[154:157], v[12:15], v[170:173], v[154:157]
	v_mfma_f32_16x16x32_f16 v[158:161], v[12:15], v[174:177], v[158:161]
	v_mfma_f32_16x16x32_f16 v[166:169], v[12:15], v[178:181], v[166:169]
	v_mfma_f32_16x16x32_f16 v[162:165], v[12:15], v[182:185], v[162:165]
	s_setprio 0
	ds_read_b128 v[170:173], v128
	ds_read_b128 v[174:177], v128 offset:2048
	ds_read_b128 v[178:181], v128 offset:4096
	ds_read_b128 v[182:185], v128 offset:6144
	ds_read_b128 v[12:15], v130
	ds_read_b128 v[40:43], v130 offset:2048
	v_cvt_pk_f16_f32 v5, v22, v23
	v_cvt_pk_f16_f32 v4, v20, v21
	ds_write_b64 v100, v[4:5] offset:49152
	s_setprio 1
	s_waitcnt lgkmcnt(1)
	v_mfma_f32_16x16x32_f16 v[0:3], v[12:15], v[170:173], v[0:3]
	v_mfma_f32_16x16x32_f16 v[4:7], v[12:15], v[174:177], v[8:11]
	v_mfma_f32_16x16x32_f16 v[8:11], v[12:15], v[178:181], v[52:55]
	v_mfma_f32_16x16x32_f16 v[12:15], v[12:15], v[182:185], v[80:83]
	v_mfma_f32_16x16x32_f16 v[16:19], v[40:43], v[170:173], v[92:95]
	v_mfma_f32_16x16x32_f16 v[20:23], v[40:43], v[174:177], v[102:105]
	v_mfma_f32_16x16x32_f16 v[36:39], v[40:43], v[178:181], v[106:109]
	v_mfma_f32_16x16x32_f16 v[40:43], v[40:43], v[182:185], v[110:113]
	s_setprio 0
	ds_read_b128 v[52:55], v130 offset:4096
	ds_read_b128 v[72:75], v130 offset:6144
	v_cvt_pk_f16_f32 v27, v26, v27
	v_cvt_pk_f16_f32 v26, v24, v25
	ds_write_b64 v100, v[26:27] offset:53248
	s_setprio 1
	s_waitcnt lgkmcnt(1)
	v_mfma_f32_16x16x32_f16 v[24:27], v[52:55], v[170:173], v[190:193]
	v_mfma_f32_16x16x32_f16 v[44:47], v[52:55], v[174:177], v[56:59]
	v_mfma_f32_16x16x32_f16 v[48:51], v[52:55], v[178:181], v[64:67]
	v_mfma_f32_16x16x32_f16 v[52:55], v[52:55], v[182:185], v[68:71]
	v_mfma_f32_16x16x32_f16 v[56:59], v[72:75], v[170:173], v[84:87]
	v_mfma_f32_16x16x32_f16 v[60:63], v[72:75], v[174:177], v[96:99]
	v_mfma_f32_16x16x32_f16 v[64:67], v[72:75], v[178:181], v[114:117]
	v_mfma_f32_16x16x32_f16 v[68:71], v[72:75], v[182:185], v[118:121]
	s_setprio 0
	ds_read_b128 v[80:83], v130 offset:8192
	ds_read_b128 v[96:99], v130 offset:10240
	v_cvt_pk_f16_f32 v31, v30, v31
	v_cvt_pk_f16_f32 v30, v28, v29
	ds_write_b64 v100, v[30:31] offset:57344
	s_setprio 1
	s_waitcnt lgkmcnt(1)
	v_mfma_f32_16x16x32_f16 v[28:31], v[80:83], v[170:173], v[122:125]
	v_mfma_f32_16x16x32_f16 v[72:75], v[80:83], v[174:177], v[186:189]
	v_mfma_f32_16x16x32_f16 v[76:79], v[80:83], v[178:181], v[202:205]
	v_mfma_f32_16x16x32_f16 v[80:83], v[80:83], v[182:185], v[88:91]
	v_mfma_f32_16x16x32_f16 v[84:87], v[96:99], v[170:173], v[134:137]
	v_mfma_f32_16x16x32_f16 v[88:91], v[96:99], v[174:177], v[138:141]
	v_mfma_f32_16x16x32_f16 v[92:95], v[96:99], v[178:181], v[146:149]
	v_mfma_f32_16x16x32_f16 v[96:99], v[96:99], v[182:185], v[142:145]
	s_setprio 0
	ds_read_b128 v[108:111], v130 offset:12288
	ds_read_b128 v[124:127], v130 offset:14336
	v_cvt_pk_f16_f32 v35, v34, v35
	v_cvt_pk_f16_f32 v34, v32, v33
	ds_write_b64 v100, v[34:35] offset:61440
	s_setprio 1
	s_waitcnt lgkmcnt(1)
	v_mfma_f32_16x16x32_f16 v[32:35], v[108:111], v[170:173], v[206:209]
	v_mfma_f32_16x16x32_f16 v[100:103], v[108:111], v[174:177], v[210:213]
	v_mfma_f32_16x16x32_f16 v[104:107], v[108:111], v[178:181], v[214:217]
	v_mfma_f32_16x16x32_f16 v[108:111], v[108:111], v[182:185], v[150:153]
	v_mfma_f32_16x16x32_f16 v[112:115], v[124:127], v[170:173], v[154:157]
	v_mfma_f32_16x16x32_f16 v[116:119], v[124:127], v[174:177], v[158:161]
	v_mfma_f32_16x16x32_f16 v[120:123], v[124:127], v[178:181], v[166:169]
	v_mfma_f32_16x16x32_f16 v[124:127], v[124:127], v[182:185], v[162:165]
	s_setprio 0
	s_waitcnt vmcnt(0)
	s_waitcnt lgkmcnt(0)
	s_barrier
	ds_read_b128 v[134:137], v131 offset:32768
	ds_read_b128 v[138:141], v131 offset:34816
	ds_read_b128 v[142:145], v131 offset:36864
	ds_read_b128 v[148:151], v131 offset:38912
	ds_read_b128 v[152:155], v129 offset:32768
	ds_read_b128 v[156:159], v129 offset:34816
	s_setprio 1
	s_waitcnt lgkmcnt(0)
	v_mfma_f32_16x16x32_f16 v[0:3], v[152:155], v[134:137], v[0:3]
	v_mfma_f32_16x16x32_f16 v[4:7], v[152:155], v[138:141], v[4:7]
	v_mfma_f32_16x16x32_f16 v[8:11], v[152:155], v[142:145], v[8:11]
	v_mfma_f32_16x16x32_f16 v[12:15], v[152:155], v[148:151], v[12:15]
	v_mfma_f32_16x16x32_f16 v[16:19], v[156:159], v[134:137], v[16:19]
	v_mfma_f32_16x16x32_f16 v[20:23], v[156:159], v[138:141], v[20:23]
	v_mfma_f32_16x16x32_f16 v[36:39], v[156:159], v[142:145], v[36:39]
	v_mfma_f32_16x16x32_f16 v[40:43], v[156:159], v[148:151], v[40:43]
	s_setprio 0
	ds_read_b128 v[152:155], v129 offset:36864
	ds_read_b128 v[156:159], v129 offset:38912
	v_and_b32_e32 v250, 0x7ffffc00, v194
	v_lshl_add_u64 v[252:253], s[10:11], 0, v[196:197]
	v_readfirstlane_b32 s32, v250
	s_nop 0
	s_mov_b32 m0, s32
	s_nop 0
	global_load_lds_dwordx4 v[252:253], off
	v_mov_b32_e32 v146, 0
	v_and_b32_e32 v251, 0xfffffff, v132
	v_cmp_gt_u32_e32 vcc, s82, v251
	v_mov_b32_e32 v132, 0
	v_mov_b32_e32 v133, 0
	s_and_saveexec_b64 s[0:1], vcc
	s_cbranch_execz .LBB1_7
	s_and_b32 s64, s78, 0x7ffffc00
	s_or_b32 s64, s64, s33
	v_or_b32_e32 v132, s64, v251
	v_mov_b32_e32 v133, v195
	v_lshl_add_u64 v[132:133], v[132:133], 2, s[12:13]
	global_load_dword v133, v[132:133], off
	v_or_b32_e32 v132, s33, v251
	v_lshlrev_b32_e32 v132, 2, v132
	global_load_dword v146, v132, s[16:17]
	s_nop 0
	global_load_dword v132, v132, s[14:15]
